# all s_setprio toggles removed from the GEMM k-loops (no priority changes)
# speedup vs baseline: 1.0013x; 1.0013x over previous
; #define PG8_AOFF(of, u) do { _Pragma("unroll") for (int hh_ = 0; hh_ < 2; ++hh_) _Pragma("unroll") for (int i_ = 0; i_ < 2; ++i_) { \
;         if constexpr (GATHER) of[hh_][i_] = (unsigned)gidx[(u).pm * 256 + hh_ * 128 + RA[i_]] * (unsigned)(lda * 2) + CA2[i_]; \
;         else of[hh_][i_] = (unsigned)((hh_ * HALF + RA[i_]) * lda) * 2u + CA2[i_]; } } while (0)
; #define PG8_STAGE(bufoff, gbase, voff) do { _Pragma("unroll") for (int _i = 0; _i < 2; ++_i) \
;         __builtin_amdgcn_global_load_lds((const unsigned*)((const char*)(gbase) + (voff)[_i]), (LAS unsigned*)(lds + (bufoff) + ldsw + _i * 8192), 16, 0, 0); } while (0)
; #define PG8_LDA(dst, b, h) do { _Pragma("unroll") for (int m = 0; m < 4; ++m) _Pragma("unroll") for (int k = 0; k < 2; ++k) dst[m][k] = *(const LAS bf16x8*)(lds + PG8_SA(b, h) + aoff + m * 2048 + k * 1024); } while (0)
; #define PG8_LDB(dst, b, h) do { _Pragma("unroll") for (int n = 0; n < 2; ++n) _Pragma("unroll") for (int k = 0; k < 2; ++k) dst[n][k] = *(const LAS bf16x8*)(lds + PG8_SB(b, h) + boff + n * 2048 + k * 1024); } while (0)
; template <class Epi, class Sched, bool GATHER = false>
; __device__ __forceinline__ void gemm_phase(LAS unsigned char* lds, const int lda, const int ldb, const int K, const Sched& S, const Epi& E, const int* gidx = nullptr) {
;     ...
;         for (int t = 0; t < nt; t += 2) {
;             const bool last = (t == nt - 2);
;             if constexpr (GATHER) { if (last && has_next) PG8_AOFF(ofn, nxt); }
;             const char* a1 = cA + (size_t)(t + 1) * kstep;
;             const char* a2 = last ? nA : cA + (size_t)(t + 2) * kstep; const char* b2 = last ? nB : cB + (size_t)(t + 2) * kstep;
;             const char* a3 = a2 + kstep; const char* b3 = b2 + kstep;
;             unsigned o2[2][2];
; #pragma unroll
;             for (int hh = 0; hh < 2; ++hh)
; #pragma unroll
;                 for (int i = 0; i < 2; ++i) { if constexpr (GATHER) o2[hh][i] = last ? ofn[hh][i] : ofc[hh][i]; else o2[hh][i] = ofc[hh][i]; }
;             PG8_LDB(B0, 0, 0); PG8_LDB(B1, 0, 1); PG8_SCHED; PG8_LDA(At, 0, 0); PG8_STAGE(PG8_SA(1, 1), a1, ofc[1]);
;             PG8_WAIT_V(8); PG8_WAIT_L(0); PG8_BAR; PG8_MMA(0, 0, At, B0); PG8_MMA(0, 1, At, B1); PG8_BAR; PG8_SCHED;
;             PG8_LDA(At, 0, 1); PG8_STAGE(PG8_SB(0, 0), b2, voffB); PG8_STAGE(PG8_SB(0, 1), b2 + hstepB, voffB); PG8_STAGE(PG8_SA(0, 0), a2, o2[0]);
.LBB0_428:
	s_add_u32 s12, s72, 0x80
	s_addc_u32 s13, s73, 0
	s_cmp_eq_u32 s75, 28
	s_cselect_b32 s67, s81, s13
	s_cselect_b32 s66, s80, s12
	s_cselect_b32 s13, s83, s74
	s_cselect_b32 s12, s82, s60
	s_add_i32 s28, 0, 0x10000
	s_add_i32 s33, 0, 0x14000
	v_add_u32_e32 v142, s28, v175
	v_add_u32_e32 v158, s33, v175
	ds_read_b128 v[126:129], v142
	ds_read_b128 v[130:133], v142 offset:1024
	ds_read_b128 v[138:141], v142 offset:2048
	ds_read_b128 v[142:145], v142 offset:3072
	ds_read_b128 v[146:149], v158
	ds_read_b128 v[150:153], v158 offset:1024
	ds_read_b128 v[154:157], v158 offset:2048
	ds_read_b128 v[158:161], v158 offset:3072
	v_lshl_add_u64 v[234:235], s[72:73], 0, v[180:181]
	s_add_i32 m0, s59, 0xc000
	ds_read_b128 v[182:185], v229
	ds_read_b128 v[186:189], v229 offset:1024
	ds_read_b128 v[190:193], v229 offset:2048
	ds_read_b128 v[196:199], v229 offset:3072
	ds_read_b128 v[200:203], v229 offset:4096
	ds_read_b128 v[204:207], v229 offset:5120
	ds_read_b128 v[208:211], v229 offset:6144
	ds_read_b128 v[230:233], v229 offset:7168
	global_load_lds_dwordx4 v[234:235], off
	v_lshl_add_u64 v[234:235], s[72:73], 0, v[178:179]
	s_add_i32 m0, s59, 0xe000
	s_nop 0
	global_load_lds_dwordx4 v[234:235], off
	s_waitcnt vmcnt(8)
	s_waitcnt lgkmcnt(0)
	s_barrier
	s_waitcnt lgkmcnt(0)
	v_mfma_f32_16x16x32_bf16 v[134:137], v[126:129], v[182:185], v[134:137]
	v_mfma_f32_16x16x32_bf16 v[122:125], v[138:141], v[182:185], v[122:125]
	v_mfma_f32_16x16x32_bf16 v[110:113], v[126:129], v[190:193], v[110:113]
	v_mfma_f32_16x16x32_bf16 v[106:109], v[138:141], v[190:193], v[106:109]
	v_mfma_f32_16x16x32_bf16 v[94:97], v[126:129], v[200:203], v[94:97]
	v_mfma_f32_16x16x32_bf16 v[90:93], v[138:141], v[200:203], v[90:93]
	v_mfma_f32_16x16x32_bf16 v[78:81], v[126:129], v[208:211], v[78:81]
	v_mfma_f32_16x16x32_bf16 v[74:77], v[138:141], v[208:211], v[74:77]
	v_mfma_f32_16x16x32_bf16 v[134:137], v[130:133], v[186:189], v[134:137]
	v_mfma_f32_16x16x32_bf16 v[122:125], v[142:145], v[186:189], v[122:125]
	v_mfma_f32_16x16x32_bf16 v[110:113], v[130:133], v[196:199], v[110:113]
	v_mfma_f32_16x16x32_bf16 v[106:109], v[142:145], v[196:199], v[106:109]
	v_mfma_f32_16x16x32_bf16 v[94:97], v[130:133], v[204:207], v[94:97]
	v_mfma_f32_16x16x32_bf16 v[90:93], v[142:145], v[204:207], v[90:93]
	v_mfma_f32_16x16x32_bf16 v[78:81], v[130:133], v[230:233], v[78:81]
	v_mfma_f32_16x16x32_bf16 v[74:77], v[142:145], v[230:233], v[74:77]
	v_mfma_f32_16x16x32_bf16 v[118:121], v[146:149], v[182:185], v[118:121]
	v_mfma_f32_16x16x32_bf16 v[114:117], v[154:157], v[182:185], v[114:117]
	v_mfma_f32_16x16x32_bf16 v[102:105], v[146:149], v[190:193], v[102:105]
	v_mfma_f32_16x16x32_bf16 v[98:101], v[154:157], v[190:193], v[98:101]
	v_mfma_f32_16x16x32_bf16 v[86:89], v[146:149], v[200:203], v[86:89]
	v_mfma_f32_16x16x32_bf16 v[82:85], v[154:157], v[200:203], v[82:85]
	v_mfma_f32_16x16x32_bf16 v[70:73], v[146:149], v[208:211], v[70:73]
	v_mfma_f32_16x16x32_bf16 v[66:69], v[154:157], v[208:211], v[66:69]
	v_mfma_f32_16x16x32_bf16 v[118:121], v[150:153], v[186:189], v[118:121]
	v_mfma_f32_16x16x32_bf16 v[114:117], v[158:161], v[186:189], v[114:117]
	v_mfma_f32_16x16x32_bf16 v[102:105], v[150:153], v[196:199], v[102:105]
	v_mfma_f32_16x16x32_bf16 v[98:101], v[158:161], v[196:199], v[98:101]
	v_mfma_f32_16x16x32_bf16 v[86:89], v[150:153], v[204:207], v[86:89]
	v_mfma_f32_16x16x32_bf16 v[82:85], v[158:161], v[204:207], v[82:85]
	v_mfma_f32_16x16x32_bf16 v[70:73], v[150:153], v[230:233], v[70:73]
	v_mfma_f32_16x16x32_bf16 v[66:69], v[158:161], v[230:233], v[66:69]
	s_barrier
	s_add_i32 s28, s28, s43
	v_lshl_add_u64 v[234:235], s[12:13], 0, v[162:163]
	s_mov_b32 m0, s28
	ds_read_b128 v[182:185], v229 offset:16384
	ds_read_b128 v[186:189], v229 offset:17408
	ds_read_b128 v[190:193], v229 offset:18432
	ds_read_b128 v[196:199], v229 offset:19456
	ds_read_b128 v[200:203], v229 offset:20480
	ds_read_b128 v[204:207], v229 offset:21504
	ds_read_b128 v[208:211], v229 offset:22528
	ds_read_b128 v[230:233], v229 offset:23552
	global_load_lds_dwordx4 v[234:235], off
	s_add_i32 m0, s28, 0x2000
	s_add_u32 s28, s12, 0x80000
	v_lshl_add_u64 v[236:237], s[12:13], 0, v[164:165]
	s_addc_u32 s29, s13, 0
	s_add_i32 s33, s33, s43
	global_load_lds_dwordx4 v[236:237], off
	v_lshl_add_u64 v[238:239], s[28:29], 0, v[162:163]
	s_mov_b32 m0, s33
	v_lshl_add_u64 v[240:241], s[66:67], 0, v[168:169]
	global_load_lds_dwordx4 v[238:239], off
	v_lshl_add_u64 v[238:239], s[28:29], 0, v[164:165]
	s_add_i32 m0, s33, 0x2000
	s_nop 0
	global_load_lds_dwordx4 v[238:239], off
	v_lshl_add_u64 v[238:239], s[66:67], 0, v[166:167]
	s_mov_b32 m0, s59
	s_nop 0
	global_load_lds_dwordx4 v[238:239], off
	s_mov_b32 m0, s36
	s_nop 0
	global_load_lds_dwordx4 v[240:241], off
	s_waitcnt vmcnt(8)
	s_waitcnt lgkmcnt(0)
	s_barrier
; #define PG8_STAGE(bufoff, gbase, voff) do { _Pragma("unroll") for (int _i = 0; _i < 2; ++_i) \
;         __builtin_amdgcn_global_load_lds((const unsigned*)((const char*)(gbase) + (voff)[_i]), (LAS unsigned*)(lds + (bufoff) + ldsw + _i * 8192), 16, 0, 0); } while (0)
; #define PG8_LDA(dst, b, h) do { _Pragma("unroll") for (int m = 0; m < 4; ++m) _Pragma("unroll") for (int k = 0; k < 2; ++k) dst[m][k] = *(const LAS bf16x8*)(lds + PG8_SA(b, h) + aoff + m * 2048 + k * 1024); } while (0)
; #define PG8_LDB(dst, b, h) do { _Pragma("unroll") for (int n = 0; n < 2; ++n) _Pragma("unroll") for (int k = 0; k < 2; ++k) dst[n][k] = *(const LAS bf16x8*)(lds + PG8_SB(b, h) + boff + n * 2048 + k * 1024); } while (0)
; #define PG8_MMA(ai, bj, At, Bt) do { __builtin_amdgcn_s_setprio(1); _Pragma("unroll") for (int m = 0; m < 4; ++m) _Pragma("unroll") for (int n = 0; n < 2; ++n) _Pragma("unroll") for (int k = 0; k < 2; ++k) \
;         acc[ai][bj][m][n] = __builtin_amdgcn_mfma_f32_16x16x32_bf16(Bt[n][k], At[m][k], acc[ai][bj][m][n], 0, 0, 0); __builtin_amdgcn_s_setprio(0); } while (0)
; #define PG8_WAIT_V(n) asm volatile("s_waitcnt vmcnt(" #n ")" ::: "memory")
; #define PG8_WAIT_L(n) asm volatile("s_waitcnt lgkmcnt(" #n ")" ::: "memory")
; #define PG8_BAR __builtin_amdgcn_s_barrier()
; #define PG8_SCHED __builtin_amdgcn_sched_barrier(0)
; template <class Epi, class Sched, bool GATHER = false>
; __device__ __forceinline__ void gemm_phase(LAS unsigned char* lds, const int lda, const int ldb, const int K, const Sched& S, const Epi& E, const int* gidx = nullptr) {
;     ...
;             PG8_WAIT_V(8); PG8_WAIT_L(0); PG8_BAR; PG8_MMA(1, 0, At, B0); PG8_MMA(1, 1, At, B1); PG8_BAR; PG8_SCHED;
;             PG8_LDB(B0, 1, 0); PG8_LDB(B1, 1, 1); PG8_SCHED; PG8_LDA(At, 1, 0); PG8_STAGE(PG8_SA(0, 1), a2, o2[1]);
;             PG8_WAIT_V(8); PG8_WAIT_L(0); PG8_BAR; PG8_MMA(0, 0, At, B0); PG8_MMA(0, 1, At, B1); PG8_BAR; PG8_SCHED;
	s_waitcnt lgkmcnt(0)
	v_mfma_f32_16x16x32_bf16 v[62:65], v[126:129], v[182:185], v[62:65]
	v_mfma_f32_16x16x32_bf16 v[58:61], v[138:141], v[182:185], v[58:61]
	v_mfma_f32_16x16x32_bf16 v[46:49], v[126:129], v[190:193], v[46:49]
	v_mfma_f32_16x16x32_bf16 v[42:45], v[138:141], v[190:193], v[42:45]
	v_mfma_f32_16x16x32_bf16 v[30:33], v[126:129], v[200:203], v[30:33]
	v_mfma_f32_16x16x32_bf16 v[26:29], v[138:141], v[200:203], v[26:29]
	v_mfma_f32_16x16x32_bf16 v[14:17], v[126:129], v[208:211], v[14:17]
	v_mfma_f32_16x16x32_bf16 v[10:13], v[138:141], v[208:211], v[10:13]
	v_mfma_f32_16x16x32_bf16 v[62:65], v[130:133], v[186:189], v[62:65]
	v_mfma_f32_16x16x32_bf16 v[58:61], v[142:145], v[186:189], v[58:61]
	v_mfma_f32_16x16x32_bf16 v[46:49], v[130:133], v[196:199], v[46:49]
	v_mfma_f32_16x16x32_bf16 v[42:45], v[142:145], v[196:199], v[42:45]
	v_mfma_f32_16x16x32_bf16 v[30:33], v[130:133], v[204:207], v[30:33]
	v_mfma_f32_16x16x32_bf16 v[26:29], v[142:145], v[204:207], v[26:29]
	v_mfma_f32_16x16x32_bf16 v[14:17], v[130:133], v[230:233], v[14:17]
	v_mfma_f32_16x16x32_bf16 v[10:13], v[142:145], v[230:233], v[10:13]
	v_mfma_f32_16x16x32_bf16 v[54:57], v[146:149], v[182:185], v[54:57]
	v_mfma_f32_16x16x32_bf16 v[50:53], v[154:157], v[182:185], v[50:53]
	v_mfma_f32_16x16x32_bf16 v[38:41], v[146:149], v[190:193], v[38:41]
	v_mfma_f32_16x16x32_bf16 v[34:37], v[154:157], v[190:193], v[34:37]
	v_mfma_f32_16x16x32_bf16 v[22:25], v[146:149], v[200:203], v[22:25]
	v_mfma_f32_16x16x32_bf16 v[18:21], v[154:157], v[200:203], v[18:21]
	v_mfma_f32_16x16x32_bf16 v[6:9], v[146:149], v[208:211], v[6:9]
	v_mfma_f32_16x16x32_bf16 v[2:5], v[154:157], v[208:211], v[2:5]
	v_mfma_f32_16x16x32_bf16 v[54:57], v[150:153], v[186:189], v[54:57]
	v_mfma_f32_16x16x32_bf16 v[50:53], v[158:161], v[186:189], v[50:53]
	v_mfma_f32_16x16x32_bf16 v[38:41], v[150:153], v[196:199], v[38:41]
	v_mfma_f32_16x16x32_bf16 v[34:37], v[158:161], v[196:199], v[34:37]
	v_mfma_f32_16x16x32_bf16 v[22:25], v[150:153], v[204:207], v[22:25]
	v_mfma_f32_16x16x32_bf16 v[18:21], v[158:161], v[204:207], v[18:21]
	v_mfma_f32_16x16x32_bf16 v[6:9], v[150:153], v[230:233], v[6:9]
	v_mfma_f32_16x16x32_bf16 v[2:5], v[158:161], v[230:233], v[2:5]
	s_barrier
	s_add_i32 s28, 0, 0x18000
	s_add_i32 s29, 0, 0x1c000
	v_add_u32_e32 v142, s28, v175
	v_add_u32_e32 v158, s29, v175
	ds_read_b128 v[126:129], v142
	ds_read_b128 v[130:133], v142 offset:1024
	ds_read_b128 v[138:141], v142 offset:2048
	ds_read_b128 v[142:145], v142 offset:3072
	ds_read_b128 v[146:149], v158
	ds_read_b128 v[150:153], v158 offset:1024
	ds_read_b128 v[154:157], v158 offset:2048
	ds_read_b128 v[158:161], v158 offset:3072
	s_mov_b32 m0, s37
	v_lshl_add_u64 v[242:243], s[66:67], 0, v[170:171]
	ds_read_b128 v[182:185], v229 offset:32768
	ds_read_b128 v[186:189], v229 offset:33792
	ds_read_b128 v[190:193], v229 offset:34816
	ds_read_b128 v[196:199], v229 offset:35840
	ds_read_b128 v[200:203], v229 offset:36864
	ds_read_b128 v[204:207], v229 offset:37888
	ds_read_b128 v[208:211], v229 offset:38912
	ds_read_b128 v[230:233], v229 offset:39936
	global_load_lds_dwordx4 v[242:243], off
	v_lshl_add_u64 v[242:243], s[66:67], 0, v[172:173]
	s_mov_b32 m0, s22
	s_nop 0
	global_load_lds_dwordx4 v[242:243], off
	s_waitcnt vmcnt(8)
	s_waitcnt lgkmcnt(0)
	s_barrier
	s_waitcnt lgkmcnt(0)
	v_mfma_f32_16x16x32_bf16 v[134:137], v[126:129], v[182:185], v[134:137]
	v_mfma_f32_16x16x32_bf16 v[122:125], v[138:141], v[182:185], v[122:125]
	v_mfma_f32_16x16x32_bf16 v[110:113], v[126:129], v[190:193], v[110:113]
	v_mfma_f32_16x16x32_bf16 v[106:109], v[138:141], v[190:193], v[106:109]
	v_mfma_f32_16x16x32_bf16 v[94:97], v[126:129], v[200:203], v[94:97]
	v_mfma_f32_16x16x32_bf16 v[90:93], v[138:141], v[200:203], v[90:93]
	v_mfma_f32_16x16x32_bf16 v[78:81], v[126:129], v[208:211], v[78:81]
	v_mfma_f32_16x16x32_bf16 v[74:77], v[138:141], v[208:211], v[74:77]
	v_mfma_f32_16x16x32_bf16 v[134:137], v[130:133], v[186:189], v[134:137]
	v_mfma_f32_16x16x32_bf16 v[122:125], v[142:145], v[186:189], v[122:125]
	v_mfma_f32_16x16x32_bf16 v[110:113], v[130:133], v[196:199], v[110:113]
	v_mfma_f32_16x16x32_bf16 v[106:109], v[142:145], v[196:199], v[106:109]
	v_mfma_f32_16x16x32_bf16 v[94:97], v[130:133], v[204:207], v[94:97]
	v_mfma_f32_16x16x32_bf16 v[90:93], v[142:145], v[204:207], v[90:93]
	v_mfma_f32_16x16x32_bf16 v[78:81], v[130:133], v[230:233], v[78:81]
	v_mfma_f32_16x16x32_bf16 v[74:77], v[142:145], v[230:233], v[74:77]
	v_mfma_f32_16x16x32_bf16 v[118:121], v[146:149], v[182:185], v[118:121]
	v_mfma_f32_16x16x32_bf16 v[114:117], v[154:157], v[182:185], v[114:117]
	v_mfma_f32_16x16x32_bf16 v[102:105], v[146:149], v[190:193], v[102:105]
	v_mfma_f32_16x16x32_bf16 v[98:101], v[154:157], v[190:193], v[98:101]
	v_mfma_f32_16x16x32_bf16 v[86:89], v[146:149], v[200:203], v[86:89]
	v_mfma_f32_16x16x32_bf16 v[82:85], v[154:157], v[200:203], v[82:85]
	v_mfma_f32_16x16x32_bf16 v[70:73], v[146:149], v[208:211], v[70:73]
	v_mfma_f32_16x16x32_bf16 v[66:69], v[154:157], v[208:211], v[66:69]
	v_mfma_f32_16x16x32_bf16 v[118:121], v[150:153], v[186:189], v[118:121]
	v_mfma_f32_16x16x32_bf16 v[114:117], v[158:161], v[186:189], v[114:117]
	v_mfma_f32_16x16x32_bf16 v[102:105], v[150:153], v[196:199], v[102:105]
	v_mfma_f32_16x16x32_bf16 v[98:101], v[158:161], v[196:199], v[98:101]
	v_mfma_f32_16x16x32_bf16 v[86:89], v[150:153], v[204:207], v[86:89]
	v_mfma_f32_16x16x32_bf16 v[82:85], v[158:161], v[204:207], v[82:85]
	v_mfma_f32_16x16x32_bf16 v[70:73], v[150:153], v[230:233], v[70:73]
	v_mfma_f32_16x16x32_bf16 v[66:69], v[158:161], v[230:233], v[66:69]
	s_barrier
; #define PG8_STAGE(bufoff, gbase, voff) do { _Pragma("unroll") for (int _i = 0; _i < 2; ++_i) \
;         __builtin_amdgcn_global_load_lds((const unsigned*)((const char*)(gbase) + (voff)[_i]), (LAS unsigned*)(lds + (bufoff) + ldsw + _i * 8192), 16, 0, 0); } while (0)
; #define PG8_LDA(dst, b, h) do { _Pragma("unroll") for (int m = 0; m < 4; ++m) _Pragma("unroll") for (int k = 0; k < 2; ++k) dst[m][k] = *(const LAS bf16x8*)(lds + PG8_SA(b, h) + aoff + m * 2048 + k * 1024); } while (0)
; #define PG8_MMA(ai, bj, At, Bt) do { __builtin_amdgcn_s_setprio(1); _Pragma("unroll") for (int m = 0; m < 4; ++m) _Pragma("unroll") for (int n = 0; n < 2; ++n) _Pragma("unroll") for (int k = 0; k < 2; ++k) \
;         acc[ai][bj][m][n] = __builtin_amdgcn_mfma_f32_16x16x32_bf16(Bt[n][k], At[m][k], acc[ai][bj][m][n], 0, 0, 0); __builtin_amdgcn_s_setprio(0); } while (0)
; #define PG8_WAIT_V(n) asm volatile("s_waitcnt vmcnt(" #n ")" ::: "memory")
; #define PG8_WAIT_L(n) asm volatile("s_waitcnt lgkmcnt(" #n ")" ::: "memory")
; #define PG8_BAR __builtin_amdgcn_s_barrier()
; #define PG8_SCHED __builtin_amdgcn_sched_barrier(0)
; template <class Epi, class Sched, bool GATHER = false>
; __device__ __forceinline__ void gemm_phase(LAS unsigned char* lds, const int lda, const int ldb, const int K, const Sched& S, const Epi& E, const int* gidx = nullptr) {
;     ...
;             PG8_LDA(At, 1, 1); PG8_STAGE(PG8_SB(1, 0), b3, voffB); PG8_STAGE(PG8_SB(1, 1), b3 + hstepB, voffB); PG8_STAGE(PG8_SA(1, 0), a3, o2[0]);
;             PG8_WAIT_V(8); PG8_WAIT_L(0); PG8_BAR; PG8_MMA(1, 0, At, B0); PG8_MMA(1, 1, At, B1); PG8_BAR; PG8_SCHED;
;         }
;         if (wr == 0) PG8_BAR;
	s_add_i32 s28, s28, s43
	v_lshl_add_u64 v[234:235], v[234:235], 0, s[64:65]
	s_mov_b32 m0, s28
	ds_read_b128 v[182:185], v229 offset:49152
	ds_read_b128 v[186:189], v229 offset:50176
	ds_read_b128 v[190:193], v229 offset:51200
	ds_read_b128 v[196:199], v229 offset:52224
	ds_read_b128 v[200:203], v229 offset:53248
	ds_read_b128 v[204:207], v229 offset:54272
	ds_read_b128 v[208:211], v229 offset:55296
	ds_read_b128 v[230:233], v229 offset:56320
	global_load_lds_dwordx4 v[234:235], off
	s_add_i32 m0, s28, 0x2000
	s_add_u32 s12, s12, 0x80080
	v_lshl_add_u64 v[234:235], v[236:237], 0, s[64:65]
	s_addc_u32 s13, s13, 0
	s_add_i32 s28, s29, s43
	global_load_lds_dwordx4 v[234:235], off
	v_lshl_add_u64 v[234:235], s[12:13], 0, v[162:163]
	s_mov_b32 m0, s28
	s_nop 0
	global_load_lds_dwordx4 v[234:235], off
	v_lshl_add_u64 v[234:235], s[12:13], 0, v[164:165]
	s_add_i32 m0, s28, 0x2000
	s_nop 0
	global_load_lds_dwordx4 v[234:235], off
	v_lshl_add_u64 v[234:235], v[238:239], 0, s[64:65]
	s_mov_b32 m0, s10
	s_nop 0
	global_load_lds_dwordx4 v[234:235], off
	v_lshl_add_u64 v[234:235], v[240:241], 0, s[64:65]
	s_mov_b32 m0, s11
	s_nop 0
	global_load_lds_dwordx4 v[234:235], off
	s_waitcnt vmcnt(8)
	s_waitcnt lgkmcnt(0)
	s_barrier
	s_waitcnt lgkmcnt(0)
	v_mfma_f32_16x16x32_bf16 v[62:65], v[126:129], v[182:185], v[62:65]
	v_mfma_f32_16x16x32_bf16 v[58:61], v[138:141], v[182:185], v[58:61]
	v_mfma_f32_16x16x32_bf16 v[46:49], v[126:129], v[190:193], v[46:49]
	v_mfma_f32_16x16x32_bf16 v[42:45], v[138:141], v[190:193], v[42:45]
	v_mfma_f32_16x16x32_bf16 v[30:33], v[126:129], v[200:203], v[30:33]
	v_mfma_f32_16x16x32_bf16 v[26:29], v[138:141], v[200:203], v[26:29]
	v_mfma_f32_16x16x32_bf16 v[14:17], v[126:129], v[208:211], v[14:17]
	v_mfma_f32_16x16x32_bf16 v[10:13], v[138:141], v[208:211], v[10:13]
	v_mfma_f32_16x16x32_bf16 v[62:65], v[130:133], v[186:189], v[62:65]
	v_mfma_f32_16x16x32_bf16 v[58:61], v[142:145], v[186:189], v[58:61]
	v_mfma_f32_16x16x32_bf16 v[46:49], v[130:133], v[196:199], v[46:49]
	v_mfma_f32_16x16x32_bf16 v[42:45], v[142:145], v[196:199], v[42:45]
	v_mfma_f32_16x16x32_bf16 v[30:33], v[130:133], v[204:207], v[30:33]
	v_mfma_f32_16x16x32_bf16 v[26:29], v[142:145], v[204:207], v[26:29]
	v_mfma_f32_16x16x32_bf16 v[14:17], v[130:133], v[230:233], v[14:17]
	v_mfma_f32_16x16x32_bf16 v[10:13], v[142:145], v[230:233], v[10:13]
	v_mfma_f32_16x16x32_bf16 v[54:57], v[146:149], v[182:185], v[54:57]
	v_mfma_f32_16x16x32_bf16 v[50:53], v[154:157], v[182:185], v[50:53]
	v_mfma_f32_16x16x32_bf16 v[38:41], v[146:149], v[190:193], v[38:41]
	v_mfma_f32_16x16x32_bf16 v[34:37], v[154:157], v[190:193], v[34:37]
	v_mfma_f32_16x16x32_bf16 v[22:25], v[146:149], v[200:203], v[22:25]
	v_mfma_f32_16x16x32_bf16 v[18:21], v[154:157], v[200:203], v[18:21]
	v_mfma_f32_16x16x32_bf16 v[6:9], v[146:149], v[208:211], v[6:9]
	v_mfma_f32_16x16x32_bf16 v[2:5], v[154:157], v[208:211], v[2:5]
	v_mfma_f32_16x16x32_bf16 v[54:57], v[150:153], v[186:189], v[54:57]
	v_mfma_f32_16x16x32_bf16 v[50:53], v[158:161], v[186:189], v[50:53]
	v_mfma_f32_16x16x32_bf16 v[38:41], v[150:153], v[196:199], v[38:41]
	v_mfma_f32_16x16x32_bf16 v[34:37], v[158:161], v[196:199], v[34:37]
	v_mfma_f32_16x16x32_bf16 v[22:25], v[150:153], v[204:207], v[22:25]
	v_mfma_f32_16x16x32_bf16 v[18:21], v[158:161], v[204:207], v[18:21]
	v_mfma_f32_16x16x32_bf16 v[6:9], v[150:153], v[230:233], v[6:9]
	v_mfma_f32_16x16x32_bf16 v[2:5], v[158:161], v[230:233], v[2:5]
	s_barrier
	s_add_i32 s75, s75, 2
	s_add_u32 s72, s72, 0x100
	s_addc_u32 s73, s73, 0
	s_add_u32 s60, s60, 0x100
	s_addc_u32 s74, s74, 0
	s_cmp_gt_u32 s75, 29
	s_cbranch_scc0 .LBB0_428
	s_and_b64 vcc, exec, s[48:49]
	s_cbranch_vccz .LBB0_431
	s_barrier

; #define PG8_AOFF(of, u) do { _Pragma("unroll") for (int hh_ = 0; hh_ < 2; ++hh_) _Pragma("unroll") for (int i_ = 0; i_ < 2; ++i_) { \
;         if constexpr (GATHER) of[hh_][i_] = (unsigned)gidx[(u).pm * 256 + hh_ * 128 + RA[i_]] * (unsigned)(lda * 2) + CA2[i_]; \
;         else of[hh_][i_] = (unsigned)((hh_ * HALF + RA[i_]) * lda) * 2u + CA2[i_]; } } while (0)
; #define PG8_STAGE(bufoff, gbase, voff) do { _Pragma("unroll") for (int _i = 0; _i < 2; ++_i) \
;         __builtin_amdgcn_global_load_lds((const unsigned*)((const char*)(gbase) + (voff)[_i]), (LAS unsigned*)(lds + (bufoff) + ldsw + _i * 8192), 16, 0, 0); } while (0)
; #define PG8_LDA(dst, b, h) do { _Pragma("unroll") for (int m = 0; m < 4; ++m) _Pragma("unroll") for (int k = 0; k < 2; ++k) dst[m][k] = *(const LAS bf16x8*)(lds + PG8_SA(b, h) + aoff + m * 2048 + k * 1024); } while (0)
; #define PG8_LDB(dst, b, h) do { _Pragma("unroll") for (int n = 0; n < 2; ++n) _Pragma("unroll") for (int k = 0; k < 2; ++k) dst[n][k] = *(const LAS bf16x8*)(lds + PG8_SB(b, h) + boff + n * 2048 + k * 1024); } while (0)
; template <class Epi, class Sched, bool GATHER = false>
; __device__ __forceinline__ void gemm_phase(LAS unsigned char* lds, const int lda, const int ldb, const int K, const Sched& S, const Epi& E, const int* gidx = nullptr) {
;     ...
;         for (int t = 0; t < nt; t += 2) {
;             const bool last = (t == nt - 2);
;             if constexpr (GATHER) { if (last && has_next) PG8_AOFF(ofn, nxt); }
;             const char* a1 = cA + (size_t)(t + 1) * kstep;
;             const char* a2 = last ? nA : cA + (size_t)(t + 2) * kstep; const char* b2 = last ? nB : cB + (size_t)(t + 2) * kstep;
;             const char* a3 = a2 + kstep; const char* b3 = b2 + kstep;
;             unsigned o2[2][2];
; #pragma unroll
;             for (int hh = 0; hh < 2; ++hh)
; #pragma unroll
;                 for (int i = 0; i < 2; ++i) { if constexpr (GATHER) o2[hh][i] = last ? ofn[hh][i] : ofc[hh][i]; else o2[hh][i] = ofc[hh][i]; }
;             PG8_LDB(B0, 0, 0); PG8_LDB(B1, 0, 1); PG8_SCHED; PG8_LDA(At, 0, 0); PG8_STAGE(PG8_SA(1, 1), a1, ofc[1]);
;             PG8_WAIT_V(8); PG8_WAIT_L(0); PG8_BAR; PG8_MMA(0, 0, At, B0); PG8_MMA(0, 1, At, B1); PG8_BAR; PG8_SCHED;
;             PG8_LDA(At, 0, 1); PG8_STAGE(PG8_SB(0, 0), b2, voffB); PG8_STAGE(PG8_SB(0, 1), b2 + hstepB, voffB); PG8_STAGE(PG8_SA(0, 0), a2, o2[0]);
.LBB0_1107:
	s_add_u32 s12, s34, 0x80
	s_addc_u32 s13, s35, 0
	s_cmp_eq_u32 s83, 28
	s_cselect_b32 s67, s71, s13
	s_cselect_b32 s66, s70, s12
	s_cselect_b32 s13, s73, s82
	s_cselect_b32 s12, s72, s69
	s_add_i32 s28, 0, 0x10000
	s_add_i32 s33, 0, 0x14000
	v_add_u32_e32 v86, s28, v178
	v_add_u32_e32 v172, s33, v178
	ds_read_b128 v[70:73], v86
	ds_read_b128 v[78:81], v86 offset:1024
	ds_read_b128 v[82:85], v86 offset:2048
	ds_read_b128 v[86:89], v86 offset:3072
	ds_read_b128 v[146:149], v172
	ds_read_b128 v[150:153], v172 offset:1024
	ds_read_b128 v[168:171], v172 offset:2048
	ds_read_b128 v[172:175], v172 offset:3072
	v_lshl_add_u64 v[176:177], s[34:35], 0, v[166:167]
	s_add_i32 m0, s59, 0xc000
	ds_read_b128 v[182:185], v180
	ds_read_b128 v[186:189], v180 offset:1024
	ds_read_b128 v[190:193], v180 offset:2048
	ds_read_b128 v[196:199], v180 offset:3072
	ds_read_b128 v[200:203], v180 offset:4096
	ds_read_b128 v[204:207], v180 offset:5120
	ds_read_b128 v[208:211], v180 offset:6144
	ds_read_b128 v[228:231], v180 offset:7168
	global_load_lds_dwordx4 v[176:177], off
	v_lshl_add_u64 v[176:177], s[34:35], 0, v[164:165]
	s_add_i32 m0, s59, 0xe000
	s_nop 0
	global_load_lds_dwordx4 v[176:177], off
	s_waitcnt vmcnt(8)
	s_waitcnt lgkmcnt(0)
	s_barrier
	s_waitcnt lgkmcnt(0)
	v_mfma_f32_16x16x32_bf16 v[142:145], v[70:73], v[182:185], v[142:145]
	v_mfma_f32_16x16x32_bf16 v[138:141], v[82:85], v[182:185], v[138:141]
	v_mfma_f32_16x16x32_bf16 v[126:129], v[70:73], v[190:193], v[126:129]
	v_mfma_f32_16x16x32_bf16 v[122:125], v[82:85], v[190:193], v[122:125]
	v_mfma_f32_16x16x32_bf16 v[110:113], v[70:73], v[200:203], v[110:113]
	v_mfma_f32_16x16x32_bf16 v[106:109], v[82:85], v[200:203], v[106:109]
	v_mfma_f32_16x16x32_bf16 v[94:97], v[70:73], v[208:211], v[94:97]
	v_mfma_f32_16x16x32_bf16 v[90:93], v[82:85], v[208:211], v[90:93]
	v_mfma_f32_16x16x32_bf16 v[142:145], v[78:81], v[186:189], v[142:145]
	v_mfma_f32_16x16x32_bf16 v[138:141], v[86:89], v[186:189], v[138:141]
	v_mfma_f32_16x16x32_bf16 v[126:129], v[78:81], v[196:199], v[126:129]
	v_mfma_f32_16x16x32_bf16 v[122:125], v[86:89], v[196:199], v[122:125]
	v_mfma_f32_16x16x32_bf16 v[110:113], v[78:81], v[204:207], v[110:113]
	v_mfma_f32_16x16x32_bf16 v[106:109], v[86:89], v[204:207], v[106:109]
	v_mfma_f32_16x16x32_bf16 v[94:97], v[78:81], v[228:231], v[94:97]
	v_mfma_f32_16x16x32_bf16 v[90:93], v[86:89], v[228:231], v[90:93]
	v_mfma_f32_16x16x32_bf16 v[134:137], v[146:149], v[182:185], v[134:137]
	v_mfma_f32_16x16x32_bf16 v[130:133], v[168:171], v[182:185], v[130:133]
	v_mfma_f32_16x16x32_bf16 v[118:121], v[146:149], v[190:193], v[118:121]
	v_mfma_f32_16x16x32_bf16 v[114:117], v[168:171], v[190:193], v[114:117]
	v_mfma_f32_16x16x32_bf16 v[102:105], v[146:149], v[200:203], v[102:105]
	v_mfma_f32_16x16x32_bf16 v[98:101], v[168:171], v[200:203], v[98:101]
	v_mfma_f32_16x16x32_bf16 v[74:77], v[146:149], v[208:211], v[74:77]
	v_mfma_f32_16x16x32_bf16 v[66:69], v[168:171], v[208:211], v[66:69]
	v_mfma_f32_16x16x32_bf16 v[134:137], v[150:153], v[186:189], v[134:137]
	v_mfma_f32_16x16x32_bf16 v[130:133], v[172:175], v[186:189], v[130:133]
	v_mfma_f32_16x16x32_bf16 v[118:121], v[150:153], v[196:199], v[118:121]
	v_mfma_f32_16x16x32_bf16 v[114:117], v[172:175], v[196:199], v[114:117]
	v_mfma_f32_16x16x32_bf16 v[102:105], v[150:153], v[204:207], v[102:105]
	v_mfma_f32_16x16x32_bf16 v[98:101], v[172:175], v[204:207], v[98:101]
	v_mfma_f32_16x16x32_bf16 v[74:77], v[150:153], v[228:231], v[74:77]
	v_mfma_f32_16x16x32_bf16 v[66:69], v[172:175], v[228:231], v[66:69]
	s_barrier
	s_add_i32 s28, s28, s8
	v_lshl_add_u64 v[176:177], s[12:13], 0, v[194:195]
	s_mov_b32 m0, s28
	ds_read_b128 v[182:185], v180 offset:16384
	ds_read_b128 v[186:189], v180 offset:17408
	ds_read_b128 v[190:193], v180 offset:18432
	ds_read_b128 v[196:199], v180 offset:19456
	ds_read_b128 v[200:203], v180 offset:20480
	ds_read_b128 v[204:207], v180 offset:21504
	ds_read_b128 v[208:211], v180 offset:22528
	ds_read_b128 v[228:231], v180 offset:23552
	global_load_lds_dwordx4 v[176:177], off
	s_add_i32 m0, s28, 0x2000
	s_add_u32 s28, s12, 0x80000
	v_lshl_add_u64 v[232:233], s[12:13], 0, v[154:155]
	s_addc_u32 s29, s13, 0
	s_add_i32 s33, s33, s8
	global_load_lds_dwordx4 v[232:233], off
	v_lshl_add_u64 v[234:235], s[28:29], 0, v[194:195]
	s_mov_b32 m0, s33
	v_lshl_add_u64 v[236:237], s[66:67], 0, v[158:159]
	global_load_lds_dwordx4 v[234:235], off
	v_lshl_add_u64 v[234:235], s[28:29], 0, v[154:155]
	s_add_i32 m0, s33, 0x2000
	s_nop 0
	global_load_lds_dwordx4 v[234:235], off
	v_lshl_add_u64 v[234:235], s[66:67], 0, v[156:157]
	s_mov_b32 m0, s59
	s_nop 0
	global_load_lds_dwordx4 v[234:235], off
	s_mov_b32 m0, s60
	s_nop 0
	global_load_lds_dwordx4 v[236:237], off
	s_waitcnt vmcnt(8)
	s_waitcnt lgkmcnt(0)
	s_barrier
; #define PG8_STAGE(bufoff, gbase, voff) do { _Pragma("unroll") for (int _i = 0; _i < 2; ++_i) \
;         __builtin_amdgcn_global_load_lds((const unsigned*)((const char*)(gbase) + (voff)[_i]), (LAS unsigned*)(lds + (bufoff) + ldsw + _i * 8192), 16, 0, 0); } while (0)
; #define PG8_LDA(dst, b, h) do { _Pragma("unroll") for (int m = 0; m < 4; ++m) _Pragma("unroll") for (int k = 0; k < 2; ++k) dst[m][k] = *(const LAS bf16x8*)(lds + PG8_SA(b, h) + aoff + m * 2048 + k * 1024); } while (0)
; #define PG8_LDB(dst, b, h) do { _Pragma("unroll") for (int n = 0; n < 2; ++n) _Pragma("unroll") for (int k = 0; k < 2; ++k) dst[n][k] = *(const LAS bf16x8*)(lds + PG8_SB(b, h) + boff + n * 2048 + k * 1024); } while (0)
; #define PG8_MMA(ai, bj, At, Bt) do { __builtin_amdgcn_s_setprio(1); _Pragma("unroll") for (int m = 0; m < 4; ++m) _Pragma("unroll") for (int n = 0; n < 2; ++n) _Pragma("unroll") for (int k = 0; k < 2; ++k) \
;         acc[ai][bj][m][n] = __builtin_amdgcn_mfma_f32_16x16x32_bf16(Bt[n][k], At[m][k], acc[ai][bj][m][n], 0, 0, 0); __builtin_amdgcn_s_setprio(0); } while (0)
; #define PG8_WAIT_V(n) asm volatile("s_waitcnt vmcnt(" #n ")" ::: "memory")
; #define PG8_WAIT_L(n) asm volatile("s_waitcnt lgkmcnt(" #n ")" ::: "memory")
; #define PG8_BAR __builtin_amdgcn_s_barrier()
; #define PG8_SCHED __builtin_amdgcn_sched_barrier(0)
; template <class Epi, class Sched, bool GATHER = false>
; __device__ __forceinline__ void gemm_phase(LAS unsigned char* lds, const int lda, const int ldb, const int K, const Sched& S, const Epi& E, const int* gidx = nullptr) {
;     ...
;             PG8_WAIT_V(8); PG8_WAIT_L(0); PG8_BAR; PG8_MMA(1, 0, At, B0); PG8_MMA(1, 1, At, B1); PG8_BAR; PG8_SCHED;
;             PG8_LDB(B0, 1, 0); PG8_LDB(B1, 1, 1); PG8_SCHED; PG8_LDA(At, 1, 0); PG8_STAGE(PG8_SA(0, 1), a2, o2[1]);
;             PG8_WAIT_V(8); PG8_WAIT_L(0); PG8_BAR; PG8_MMA(0, 0, At, B0); PG8_MMA(0, 1, At, B1); PG8_BAR; PG8_SCHED;
	s_waitcnt lgkmcnt(0)
	v_mfma_f32_16x16x32_bf16 v[62:65], v[70:73], v[182:185], v[62:65]
	v_mfma_f32_16x16x32_bf16 v[58:61], v[82:85], v[182:185], v[58:61]
	v_mfma_f32_16x16x32_bf16 v[46:49], v[70:73], v[190:193], v[46:49]
	v_mfma_f32_16x16x32_bf16 v[38:41], v[82:85], v[190:193], v[38:41]
	v_mfma_f32_16x16x32_bf16 v[26:29], v[70:73], v[200:203], v[26:29]
	v_mfma_f32_16x16x32_bf16 v[18:21], v[82:85], v[200:203], v[18:21]
	v_mfma_f32_16x16x32_bf16 v[6:9], v[70:73], v[208:211], v[6:9]
	v_mfma_f32_16x16x32_bf16 v[2:5], v[82:85], v[208:211], v[2:5]
	v_mfma_f32_16x16x32_bf16 v[62:65], v[78:81], v[186:189], v[62:65]
	v_mfma_f32_16x16x32_bf16 v[58:61], v[86:89], v[186:189], v[58:61]
	v_mfma_f32_16x16x32_bf16 v[46:49], v[78:81], v[196:199], v[46:49]
	v_mfma_f32_16x16x32_bf16 v[38:41], v[86:89], v[196:199], v[38:41]
	v_mfma_f32_16x16x32_bf16 v[26:29], v[78:81], v[204:207], v[26:29]
	v_mfma_f32_16x16x32_bf16 v[18:21], v[86:89], v[204:207], v[18:21]
	v_mfma_f32_16x16x32_bf16 v[6:9], v[78:81], v[228:231], v[6:9]
	v_mfma_f32_16x16x32_bf16 v[2:5], v[86:89], v[228:231], v[2:5]
	v_mfma_f32_16x16x32_bf16 v[54:57], v[146:149], v[182:185], v[54:57]
	v_mfma_f32_16x16x32_bf16 v[50:53], v[168:171], v[182:185], v[50:53]
	v_mfma_f32_16x16x32_bf16 v[42:45], v[146:149], v[190:193], v[42:45]
	v_mfma_f32_16x16x32_bf16 v[34:37], v[168:171], v[190:193], v[34:37]
	v_mfma_f32_16x16x32_bf16 v[30:33], v[146:149], v[200:203], v[30:33]
	v_mfma_f32_16x16x32_bf16 v[22:25], v[168:171], v[200:203], v[22:25]
	v_mfma_f32_16x16x32_bf16 v[14:17], v[146:149], v[208:211], v[14:17]
	v_mfma_f32_16x16x32_bf16 v[10:13], v[168:171], v[208:211], v[10:13]
	v_mfma_f32_16x16x32_bf16 v[54:57], v[150:153], v[186:189], v[54:57]
	v_mfma_f32_16x16x32_bf16 v[50:53], v[172:175], v[186:189], v[50:53]
	v_mfma_f32_16x16x32_bf16 v[42:45], v[150:153], v[196:199], v[42:45]
	v_mfma_f32_16x16x32_bf16 v[34:37], v[172:175], v[196:199], v[34:37]
	v_mfma_f32_16x16x32_bf16 v[30:33], v[150:153], v[204:207], v[30:33]
	v_mfma_f32_16x16x32_bf16 v[22:25], v[172:175], v[204:207], v[22:25]
	v_mfma_f32_16x16x32_bf16 v[14:17], v[150:153], v[228:231], v[14:17]
	v_mfma_f32_16x16x32_bf16 v[10:13], v[172:175], v[228:231], v[10:13]
	s_barrier
	s_add_i32 s28, 0, 0x18000
	s_add_i32 s29, 0, 0x1c000
	v_add_u32_e32 v86, s28, v178
	v_add_u32_e32 v172, s29, v178
	ds_read_b128 v[70:73], v86
	ds_read_b128 v[78:81], v86 offset:1024
	ds_read_b128 v[82:85], v86 offset:2048
	ds_read_b128 v[86:89], v86 offset:3072
	ds_read_b128 v[146:149], v172
	ds_read_b128 v[150:153], v172 offset:1024
	ds_read_b128 v[168:171], v172 offset:2048
	ds_read_b128 v[172:175], v172 offset:3072
	s_mov_b32 m0, s74
	v_lshl_add_u64 v[238:239], s[66:67], 0, v[160:161]
	ds_read_b128 v[182:185], v180 offset:32768
	ds_read_b128 v[186:189], v180 offset:33792
	ds_read_b128 v[190:193], v180 offset:34816
	ds_read_b128 v[196:199], v180 offset:35840
	ds_read_b128 v[200:203], v180 offset:36864
	ds_read_b128 v[204:207], v180 offset:37888
	ds_read_b128 v[208:211], v180 offset:38912
	ds_read_b128 v[228:231], v180 offset:39936
	global_load_lds_dwordx4 v[238:239], off
	v_lshl_add_u64 v[238:239], s[66:67], 0, v[162:163]
	s_mov_b32 m0, s75
	s_nop 0
	global_load_lds_dwordx4 v[238:239], off
	s_waitcnt vmcnt(8)
	s_waitcnt lgkmcnt(0)
	s_barrier
	s_waitcnt lgkmcnt(0)
	v_mfma_f32_16x16x32_bf16 v[142:145], v[70:73], v[182:185], v[142:145]
	v_mfma_f32_16x16x32_bf16 v[138:141], v[82:85], v[182:185], v[138:141]
	v_mfma_f32_16x16x32_bf16 v[126:129], v[70:73], v[190:193], v[126:129]
	v_mfma_f32_16x16x32_bf16 v[122:125], v[82:85], v[190:193], v[122:125]
	v_mfma_f32_16x16x32_bf16 v[110:113], v[70:73], v[200:203], v[110:113]
	v_mfma_f32_16x16x32_bf16 v[106:109], v[82:85], v[200:203], v[106:109]
	v_mfma_f32_16x16x32_bf16 v[94:97], v[70:73], v[208:211], v[94:97]
	v_mfma_f32_16x16x32_bf16 v[90:93], v[82:85], v[208:211], v[90:93]
	v_mfma_f32_16x16x32_bf16 v[142:145], v[78:81], v[186:189], v[142:145]
	v_mfma_f32_16x16x32_bf16 v[138:141], v[86:89], v[186:189], v[138:141]
	v_mfma_f32_16x16x32_bf16 v[126:129], v[78:81], v[196:199], v[126:129]
	v_mfma_f32_16x16x32_bf16 v[122:125], v[86:89], v[196:199], v[122:125]
	v_mfma_f32_16x16x32_bf16 v[110:113], v[78:81], v[204:207], v[110:113]
	v_mfma_f32_16x16x32_bf16 v[106:109], v[86:89], v[204:207], v[106:109]
	v_mfma_f32_16x16x32_bf16 v[94:97], v[78:81], v[228:231], v[94:97]
	v_mfma_f32_16x16x32_bf16 v[90:93], v[86:89], v[228:231], v[90:93]
	v_mfma_f32_16x16x32_bf16 v[134:137], v[146:149], v[182:185], v[134:137]
	v_mfma_f32_16x16x32_bf16 v[130:133], v[168:171], v[182:185], v[130:133]
	v_mfma_f32_16x16x32_bf16 v[118:121], v[146:149], v[190:193], v[118:121]
	v_mfma_f32_16x16x32_bf16 v[114:117], v[168:171], v[190:193], v[114:117]
	v_mfma_f32_16x16x32_bf16 v[102:105], v[146:149], v[200:203], v[102:105]
	v_mfma_f32_16x16x32_bf16 v[98:101], v[168:171], v[200:203], v[98:101]
	v_mfma_f32_16x16x32_bf16 v[74:77], v[146:149], v[208:211], v[74:77]
	v_mfma_f32_16x16x32_bf16 v[66:69], v[168:171], v[208:211], v[66:69]
	v_mfma_f32_16x16x32_bf16 v[134:137], v[150:153], v[186:189], v[134:137]
	v_mfma_f32_16x16x32_bf16 v[130:133], v[172:175], v[186:189], v[130:133]
	v_mfma_f32_16x16x32_bf16 v[118:121], v[150:153], v[196:199], v[118:121]
	v_mfma_f32_16x16x32_bf16 v[114:117], v[172:175], v[196:199], v[114:117]
	v_mfma_f32_16x16x32_bf16 v[102:105], v[150:153], v[204:207], v[102:105]
	v_mfma_f32_16x16x32_bf16 v[98:101], v[172:175], v[204:207], v[98:101]
	v_mfma_f32_16x16x32_bf16 v[74:77], v[150:153], v[228:231], v[74:77]
	v_mfma_f32_16x16x32_bf16 v[66:69], v[172:175], v[228:231], v[66:69]
	s_barrier
; #define PG8_STAGE(bufoff, gbase, voff) do { _Pragma("unroll") for (int _i = 0; _i < 2; ++_i) \
;         __builtin_amdgcn_global_load_lds((const unsigned*)((const char*)(gbase) + (voff)[_i]), (LAS unsigned*)(lds + (bufoff) + ldsw + _i * 8192), 16, 0, 0); } while (0)
; #define PG8_LDA(dst, b, h) do { _Pragma("unroll") for (int m = 0; m < 4; ++m) _Pragma("unroll") for (int k = 0; k < 2; ++k) dst[m][k] = *(const LAS bf16x8*)(lds + PG8_SA(b, h) + aoff + m * 2048 + k * 1024); } while (0)
; #define PG8_MMA(ai, bj, At, Bt) do { __builtin_amdgcn_s_setprio(1); _Pragma("unroll") for (int m = 0; m < 4; ++m) _Pragma("unroll") for (int n = 0; n < 2; ++n) _Pragma("unroll") for (int k = 0; k < 2; ++k) \
;         acc[ai][bj][m][n] = __builtin_amdgcn_mfma_f32_16x16x32_bf16(Bt[n][k], At[m][k], acc[ai][bj][m][n], 0, 0, 0); __builtin_amdgcn_s_setprio(0); } while (0)
; #define PG8_WAIT_V(n) asm volatile("s_waitcnt vmcnt(" #n ")" ::: "memory")
; #define PG8_WAIT_L(n) asm volatile("s_waitcnt lgkmcnt(" #n ")" ::: "memory")
; #define PG8_BAR __builtin_amdgcn_s_barrier()
; #define PG8_SCHED __builtin_amdgcn_sched_barrier(0)
; template <class Epi, class Sched, bool GATHER = false>
; __device__ __forceinline__ void gemm_phase(LAS unsigned char* lds, const int lda, const int ldb, const int K, const Sched& S, const Epi& E, const int* gidx = nullptr) {
;     ...
;             PG8_LDA(At, 1, 1); PG8_STAGE(PG8_SB(1, 0), b3, voffB); PG8_STAGE(PG8_SB(1, 1), b3 + hstepB, voffB); PG8_STAGE(PG8_SA(1, 0), a3, o2[0]);
;             PG8_WAIT_V(8); PG8_WAIT_L(0); PG8_BAR; PG8_MMA(1, 0, At, B0); PG8_MMA(1, 1, At, B1); PG8_BAR; PG8_SCHED;
;         }
;         if (wr == 0) PG8_BAR;
	s_add_i32 s28, s28, s8
	v_lshl_add_u64 v[176:177], v[176:177], 0, s[64:65]
	s_mov_b32 m0, s28
	ds_read_b128 v[182:185], v180 offset:49152
	ds_read_b128 v[186:189], v180 offset:50176
	ds_read_b128 v[190:193], v180 offset:51200
	ds_read_b128 v[196:199], v180 offset:52224
	ds_read_b128 v[200:203], v180 offset:53248
	ds_read_b128 v[204:207], v180 offset:54272
	ds_read_b128 v[208:211], v180 offset:55296
	ds_read_b128 v[228:231], v180 offset:56320
	global_load_lds_dwordx4 v[176:177], off
	s_add_i32 m0, s28, 0x2000
	s_add_u32 s12, s12, 0x80080
	v_lshl_add_u64 v[176:177], v[232:233], 0, s[64:65]
	s_addc_u32 s13, s13, 0
	s_add_i32 s28, s29, s8
	global_load_lds_dwordx4 v[176:177], off
	v_lshl_add_u64 v[176:177], s[12:13], 0, v[194:195]
	s_mov_b32 m0, s28
	s_nop 0
	global_load_lds_dwordx4 v[176:177], off
	v_lshl_add_u64 v[176:177], s[12:13], 0, v[154:155]
	s_add_i32 m0, s28, 0x2000
	s_nop 0
	global_load_lds_dwordx4 v[176:177], off
	v_lshl_add_u64 v[176:177], v[234:235], 0, s[64:65]
	s_mov_b32 m0, s76
	s_nop 0
	global_load_lds_dwordx4 v[176:177], off
	v_lshl_add_u64 v[176:177], v[236:237], 0, s[64:65]
	s_mov_b32 m0, s77
	s_nop 0
	global_load_lds_dwordx4 v[176:177], off
	s_waitcnt vmcnt(8)
	s_waitcnt lgkmcnt(0)
	s_barrier
	s_waitcnt lgkmcnt(0)
	v_mfma_f32_16x16x32_bf16 v[62:65], v[70:73], v[182:185], v[62:65]
	v_mfma_f32_16x16x32_bf16 v[58:61], v[82:85], v[182:185], v[58:61]
	v_mfma_f32_16x16x32_bf16 v[46:49], v[70:73], v[190:193], v[46:49]
	v_mfma_f32_16x16x32_bf16 v[38:41], v[82:85], v[190:193], v[38:41]
	v_mfma_f32_16x16x32_bf16 v[26:29], v[70:73], v[200:203], v[26:29]
	v_mfma_f32_16x16x32_bf16 v[18:21], v[82:85], v[200:203], v[18:21]
	v_mfma_f32_16x16x32_bf16 v[6:9], v[70:73], v[208:211], v[6:9]
	v_mfma_f32_16x16x32_bf16 v[2:5], v[82:85], v[208:211], v[2:5]
	v_mfma_f32_16x16x32_bf16 v[62:65], v[78:81], v[186:189], v[62:65]
	v_mfma_f32_16x16x32_bf16 v[58:61], v[86:89], v[186:189], v[58:61]
	v_mfma_f32_16x16x32_bf16 v[46:49], v[78:81], v[196:199], v[46:49]
	v_mfma_f32_16x16x32_bf16 v[38:41], v[86:89], v[196:199], v[38:41]
	v_mfma_f32_16x16x32_bf16 v[26:29], v[78:81], v[204:207], v[26:29]
	v_mfma_f32_16x16x32_bf16 v[18:21], v[86:89], v[204:207], v[18:21]
	v_mfma_f32_16x16x32_bf16 v[6:9], v[78:81], v[228:231], v[6:9]
	v_mfma_f32_16x16x32_bf16 v[2:5], v[86:89], v[228:231], v[2:5]
	v_mfma_f32_16x16x32_bf16 v[54:57], v[146:149], v[182:185], v[54:57]
	v_mfma_f32_16x16x32_bf16 v[50:53], v[168:171], v[182:185], v[50:53]
	v_mfma_f32_16x16x32_bf16 v[42:45], v[146:149], v[190:193], v[42:45]
	v_mfma_f32_16x16x32_bf16 v[34:37], v[168:171], v[190:193], v[34:37]
	v_mfma_f32_16x16x32_bf16 v[30:33], v[146:149], v[200:203], v[30:33]
	v_mfma_f32_16x16x32_bf16 v[22:25], v[168:171], v[200:203], v[22:25]
	v_mfma_f32_16x16x32_bf16 v[14:17], v[146:149], v[208:211], v[14:17]
	v_mfma_f32_16x16x32_bf16 v[10:13], v[168:171], v[208:211], v[10:13]
	v_mfma_f32_16x16x32_bf16 v[54:57], v[150:153], v[186:189], v[54:57]
	v_mfma_f32_16x16x32_bf16 v[50:53], v[172:175], v[186:189], v[50:53]
	v_mfma_f32_16x16x32_bf16 v[42:45], v[150:153], v[196:199], v[42:45]
	v_mfma_f32_16x16x32_bf16 v[34:37], v[172:175], v[196:199], v[34:37]
	v_mfma_f32_16x16x32_bf16 v[30:33], v[150:153], v[204:207], v[30:33]
	v_mfma_f32_16x16x32_bf16 v[22:25], v[172:175], v[204:207], v[22:25]
	v_mfma_f32_16x16x32_bf16 v[14:17], v[150:153], v[228:231], v[14:17]
	v_mfma_f32_16x16x32_bf16 v[10:13], v[172:175], v[228:231], v[10:13]
	s_barrier
	s_add_i32 s83, s83, 2
	s_add_u32 s34, s34, 0x100
	s_addc_u32 s35, s35, 0
	s_add_u32 s69, s69, 0x100
	s_addc_u32 s82, s82, 0
	s_cmp_gt_u32 s83, 29
	s_cbranch_scc0 .LBB0_1107
	s_and_b64 vcc, exec, s[48:49]
	s_cbranch_vccz .LBB0_1110
	s_barrier

; #define PG8_AOFF(of, u) do { _Pragma("unroll") for (int hh_ = 0; hh_ < 2; ++hh_) _Pragma("unroll") for (int i_ = 0; i_ < 2; ++i_) { \
;         if constexpr (GATHER) of[hh_][i_] = (unsigned)gidx[(u).pm * 256 + hh_ * 128 + RA[i_]] * (unsigned)(lda * 2) + CA2[i_]; \
;         else of[hh_][i_] = (unsigned)((hh_ * HALF + RA[i_]) * lda) * 2u + CA2[i_]; } } while (0)
; #define PG8_STAGE(bufoff, gbase, voff) do { _Pragma("unroll") for (int _i = 0; _i < 2; ++_i) \
;         __builtin_amdgcn_global_load_lds((const unsigned*)((const char*)(gbase) + (voff)[_i]), (LAS unsigned*)(lds + (bufoff) + ldsw + _i * 8192), 16, 0, 0); } while (0)
; #define PG8_LDA(dst, b, h) do { _Pragma("unroll") for (int m = 0; m < 4; ++m) _Pragma("unroll") for (int k = 0; k < 2; ++k) dst[m][k] = *(const LAS bf16x8*)(lds + PG8_SA(b, h) + aoff + m * 2048 + k * 1024); } while (0)
; #define PG8_LDB(dst, b, h) do { _Pragma("unroll") for (int n = 0; n < 2; ++n) _Pragma("unroll") for (int k = 0; k < 2; ++k) dst[n][k] = *(const LAS bf16x8*)(lds + PG8_SB(b, h) + boff + n * 2048 + k * 1024); } while (0)
; template <class Epi, class Sched, bool GATHER = false>
; __device__ __forceinline__ void gemm_phase(LAS unsigned char* lds, const int lda, const int ldb, const int K, const Sched& S, const Epi& E, const int* gidx = nullptr) {
;     ...
;         for (int t = 0; t < nt; t += 2) {
;             const bool last = (t == nt - 2);
;             if constexpr (GATHER) { if (last && has_next) PG8_AOFF(ofn, nxt); }
;             const char* a1 = cA + (size_t)(t + 1) * kstep;
;             const char* a2 = last ? nA : cA + (size_t)(t + 2) * kstep; const char* b2 = last ? nB : cB + (size_t)(t + 2) * kstep;
;             const char* a3 = a2 + kstep; const char* b3 = b2 + kstep;
;             unsigned o2[2][2];
; #pragma unroll
;             for (int hh = 0; hh < 2; ++hh)
; #pragma unroll
;                 for (int i = 0; i < 2; ++i) { if constexpr (GATHER) o2[hh][i] = last ? ofn[hh][i] : ofc[hh][i]; else o2[hh][i] = ofc[hh][i]; }
;             PG8_LDB(B0, 0, 0); PG8_LDB(B1, 0, 1); PG8_SCHED; PG8_LDA(At, 0, 0); PG8_STAGE(PG8_SA(1, 1), a1, ofc[1]);
;             PG8_WAIT_V(8); PG8_WAIT_L(0); PG8_BAR; PG8_MMA(0, 0, At, B0); PG8_MMA(0, 1, At, B1); PG8_BAR; PG8_SCHED;
;             PG8_LDA(At, 0, 1); PG8_STAGE(PG8_SB(0, 0), b2, voffB); PG8_STAGE(PG8_SB(0, 1), b2 + hstepB, voffB); PG8_STAGE(PG8_SA(0, 0), a2, o2[0]);
.LBB0_1186:
	s_add_u32 s28, s74, s12
	s_addc_u32 s29, s75, s13
	s_add_u32 s28, s28, 0x100
	s_addc_u32 s29, s29, 0
	s_add_u32 s33, s68, s12
	s_addc_u32 s34, s69, s13
	s_cmpk_eq_i32 s12, 0xf00
	s_cselect_b32 s49, s75, s29
	s_cselect_b32 s48, s74, s28
	s_cselect_b32 s35, s45, s34
	s_cselect_b32 s34, s44, s33
	s_add_i32 s28, 0, 0x10000
	s_add_i32 s33, 0, 0x14000
	v_add_u32_e32 v102, s28, v84
	v_add_u32_e32 v118, s33, v84
	ds_read_b128 v[90:93], v102
	ds_read_b128 v[94:97], v102 offset:1024
	ds_read_b128 v[98:101], v102 offset:2048
	ds_read_b128 v[102:105], v102 offset:3072
	ds_read_b128 v[106:109], v118
	ds_read_b128 v[110:113], v118 offset:1024
	ds_read_b128 v[114:117], v118 offset:2048
	ds_read_b128 v[118:121], v118 offset:3072
	v_lshl_add_u64 v[204:205], v[82:83], 0, s[12:13]
	s_add_i32 m0, s51, 0xc000
	ds_read_b128 v[130:133], v85
	ds_read_b128 v[134:137], v85 offset:1024
	ds_read_b128 v[186:189], v85 offset:2048
	ds_read_b128 v[190:193], v85 offset:3072
	ds_read_b128 v[196:199], v85 offset:4096
	ds_read_b128 v[200:203], v85 offset:5120
	ds_read_b128 v[208:211], v85 offset:6144
	ds_read_b128 v[228:231], v85 offset:7168
	global_load_lds_dwordx4 v[204:205], off
	v_lshl_add_u64 v[204:205], v[80:81], 0, s[12:13]
	s_add_i32 m0, s51, 0xe000
	s_nop 0
	global_load_lds_dwordx4 v[204:205], off
	s_waitcnt vmcnt(8)
	s_waitcnt lgkmcnt(0)
	s_barrier
	s_waitcnt lgkmcnt(0)
	v_mfma_f32_16x16x32_bf16 v[182:185], v[90:93], v[130:133], v[182:185]
	v_mfma_f32_16x16x32_bf16 v[178:181], v[98:101], v[130:133], v[178:181]
	v_mfma_f32_16x16x32_bf16 v[166:169], v[90:93], v[186:189], v[166:169]
	v_mfma_f32_16x16x32_bf16 v[162:165], v[98:101], v[186:189], v[162:165]
	v_mfma_f32_16x16x32_bf16 v[150:153], v[90:93], v[196:199], v[150:153]
	v_mfma_f32_16x16x32_bf16 v[146:149], v[98:101], v[196:199], v[146:149]
	v_mfma_f32_16x16x32_bf16 v[126:129], v[90:93], v[208:211], v[126:129]
	v_mfma_f32_16x16x32_bf16 v[122:125], v[98:101], v[208:211], v[122:125]
	v_mfma_f32_16x16x32_bf16 v[182:185], v[94:97], v[134:137], v[182:185]
	v_mfma_f32_16x16x32_bf16 v[178:181], v[102:105], v[134:137], v[178:181]
	v_mfma_f32_16x16x32_bf16 v[166:169], v[94:97], v[190:193], v[166:169]
	v_mfma_f32_16x16x32_bf16 v[162:165], v[102:105], v[190:193], v[162:165]
	v_mfma_f32_16x16x32_bf16 v[150:153], v[94:97], v[200:203], v[150:153]
	v_mfma_f32_16x16x32_bf16 v[146:149], v[102:105], v[200:203], v[146:149]
	v_mfma_f32_16x16x32_bf16 v[126:129], v[94:97], v[228:231], v[126:129]
	v_mfma_f32_16x16x32_bf16 v[122:125], v[102:105], v[228:231], v[122:125]
	v_mfma_f32_16x16x32_bf16 v[174:177], v[106:109], v[130:133], v[174:177]
	v_mfma_f32_16x16x32_bf16 v[130:133], v[114:117], v[130:133], v[170:173]
	v_mfma_f32_16x16x32_bf16 v[154:157], v[114:117], v[186:189], v[154:157]
	v_mfma_f32_16x16x32_bf16 v[142:145], v[106:109], v[196:199], v[142:145]
	v_mfma_f32_16x16x32_bf16 v[138:141], v[114:117], v[196:199], v[138:141]
	v_mfma_f32_16x16x32_bf16 v[86:89], v[106:109], v[208:211], v[86:89]
	v_mfma_f32_16x16x32_bf16 v[74:77], v[114:117], v[208:211], v[74:77]
	v_mfma_f32_16x16x32_bf16 v[174:177], v[110:113], v[134:137], v[174:177]
	v_mfma_f32_16x16x32_bf16 v[130:133], v[118:121], v[134:137], v[130:133]
	v_mfma_f32_16x16x32_bf16 v[134:137], v[106:109], v[186:189], v[158:161]
	v_mfma_f32_16x16x32_bf16 v[154:157], v[118:121], v[190:193], v[154:157]
	v_mfma_f32_16x16x32_bf16 v[142:145], v[110:113], v[200:203], v[142:145]
	v_mfma_f32_16x16x32_bf16 v[138:141], v[118:121], v[200:203], v[138:141]
	v_mfma_f32_16x16x32_bf16 v[86:89], v[110:113], v[228:231], v[86:89]
	v_mfma_f32_16x16x32_bf16 v[74:77], v[118:121], v[228:231], v[74:77]
	v_mfma_f32_16x16x32_bf16 v[134:137], v[110:113], v[190:193], v[134:137]
	s_barrier
	s_add_i32 s28, s28, s50
	v_lshl_add_u64 v[204:205], s[34:35], 0, v[194:195]
	s_mov_b32 m0, s28
	ds_read_b128 v[158:161], v85 offset:16384
	ds_read_b128 v[170:173], v85 offset:17408
	ds_read_b128 v[186:189], v85 offset:18432
	ds_read_b128 v[190:193], v85 offset:19456
	ds_read_b128 v[196:199], v85 offset:20480
	ds_read_b128 v[200:203], v85 offset:21504
	ds_read_b128 v[208:211], v85 offset:22528
	ds_read_b128 v[228:231], v85 offset:23552
	global_load_lds_dwordx4 v[204:205], off
	s_add_i32 m0, s28, 0x2000
	s_add_u32 s28, s34, 0x80000
	v_lshl_add_u64 v[232:233], s[34:35], 0, v[2:3]
	s_addc_u32 s29, s35, 0
	s_add_i32 s33, s33, s50
	global_load_lds_dwordx4 v[232:233], off
	v_lshl_add_u64 v[234:235], s[28:29], 0, v[194:195]
	s_mov_b32 m0, s33
	v_lshl_add_u64 v[236:237], s[48:49], 0, v[6:7]
	global_load_lds_dwordx4 v[234:235], off
	v_lshl_add_u64 v[234:235], s[28:29], 0, v[2:3]
	s_add_i32 m0, s33, 0x2000
	s_nop 0
	global_load_lds_dwordx4 v[234:235], off
	v_lshl_add_u64 v[234:235], s[48:49], 0, v[4:5]
	s_mov_b32 m0, s51
	s_nop 0
	global_load_lds_dwordx4 v[234:235], off
	s_mov_b32 m0, s60
	s_nop 0
	global_load_lds_dwordx4 v[236:237], off
	s_waitcnt vmcnt(8)
	s_waitcnt lgkmcnt(0)
	s_barrier
; #define PG8_STAGE(bufoff, gbase, voff) do { _Pragma("unroll") for (int _i = 0; _i < 2; ++_i) \
;         __builtin_amdgcn_global_load_lds((const unsigned*)((const char*)(gbase) + (voff)[_i]), (LAS unsigned*)(lds + (bufoff) + ldsw + _i * 8192), 16, 0, 0); } while (0)
; #define PG8_LDA(dst, b, h) do { _Pragma("unroll") for (int m = 0; m < 4; ++m) _Pragma("unroll") for (int k = 0; k < 2; ++k) dst[m][k] = *(const LAS bf16x8*)(lds + PG8_SA(b, h) + aoff + m * 2048 + k * 1024); } while (0)
; #define PG8_LDB(dst, b, h) do { _Pragma("unroll") for (int n = 0; n < 2; ++n) _Pragma("unroll") for (int k = 0; k < 2; ++k) dst[n][k] = *(const LAS bf16x8*)(lds + PG8_SB(b, h) + boff + n * 2048 + k * 1024); } while (0)
; #define PG8_MMA(ai, bj, At, Bt) do { __builtin_amdgcn_s_setprio(1); _Pragma("unroll") for (int m = 0; m < 4; ++m) _Pragma("unroll") for (int n = 0; n < 2; ++n) _Pragma("unroll") for (int k = 0; k < 2; ++k) \
;         acc[ai][bj][m][n] = __builtin_amdgcn_mfma_f32_16x16x32_bf16(Bt[n][k], At[m][k], acc[ai][bj][m][n], 0, 0, 0); __builtin_amdgcn_s_setprio(0); } while (0)
; #define PG8_WAIT_V(n) asm volatile("s_waitcnt vmcnt(" #n ")" ::: "memory")
; #define PG8_WAIT_L(n) asm volatile("s_waitcnt lgkmcnt(" #n ")" ::: "memory")
; #define PG8_BAR __builtin_amdgcn_s_barrier()
; #define PG8_SCHED __builtin_amdgcn_sched_barrier(0)
; template <class Epi, class Sched, bool GATHER = false>
; __device__ __forceinline__ void gemm_phase(LAS unsigned char* lds, const int lda, const int ldb, const int K, const Sched& S, const Epi& E, const int* gidx = nullptr) {
;     ...
;             PG8_WAIT_V(8); PG8_WAIT_L(0); PG8_BAR; PG8_MMA(1, 0, At, B0); PG8_MMA(1, 1, At, B1); PG8_BAR; PG8_SCHED;
;             PG8_LDB(B0, 1, 0); PG8_LDB(B1, 1, 1); PG8_SCHED; PG8_LDA(At, 1, 0); PG8_STAGE(PG8_SA(0, 1), a2, o2[1]);
;             PG8_WAIT_V(8); PG8_WAIT_L(0); PG8_BAR; PG8_MMA(0, 0, At, B0); PG8_MMA(0, 1, At, B1); PG8_BAR; PG8_SCHED;
	s_waitcnt lgkmcnt(0)
	v_mfma_f32_16x16x32_bf16 v[70:73], v[90:93], v[158:161], v[70:73]
	v_mfma_f32_16x16x32_bf16 v[66:69], v[98:101], v[158:161], v[66:69]
	v_mfma_f32_16x16x32_bf16 v[54:57], v[90:93], v[186:189], v[54:57]
	v_mfma_f32_16x16x32_bf16 v[46:49], v[98:101], v[186:189], v[46:49]
	v_mfma_f32_16x16x32_bf16 v[34:37], v[90:93], v[196:199], v[34:37]
	v_mfma_f32_16x16x32_bf16 v[26:29], v[98:101], v[196:199], v[26:29]
	v_mfma_f32_16x16x32_bf16 v[22:25], v[90:93], v[208:211], v[22:25]
	v_mfma_f32_16x16x32_bf16 v[18:21], v[98:101], v[208:211], v[18:21]
	v_mfma_f32_16x16x32_bf16 v[70:73], v[94:97], v[170:173], v[70:73]
	v_mfma_f32_16x16x32_bf16 v[66:69], v[102:105], v[170:173], v[66:69]
	v_mfma_f32_16x16x32_bf16 v[54:57], v[94:97], v[190:193], v[54:57]
	v_mfma_f32_16x16x32_bf16 v[46:49], v[102:105], v[190:193], v[46:49]
	v_mfma_f32_16x16x32_bf16 v[34:37], v[94:97], v[200:203], v[34:37]
	v_mfma_f32_16x16x32_bf16 v[26:29], v[102:105], v[200:203], v[26:29]
	v_mfma_f32_16x16x32_bf16 v[22:25], v[94:97], v[228:231], v[22:25]
	v_mfma_f32_16x16x32_bf16 v[18:21], v[102:105], v[228:231], v[18:21]
	v_mfma_f32_16x16x32_bf16 v[62:65], v[106:109], v[158:161], v[62:65]
	v_mfma_f32_16x16x32_bf16 v[58:61], v[114:117], v[158:161], v[58:61]
	v_mfma_f32_16x16x32_bf16 v[50:53], v[106:109], v[186:189], v[50:53]
	v_mfma_f32_16x16x32_bf16 v[42:45], v[114:117], v[186:189], v[42:45]
	v_mfma_f32_16x16x32_bf16 v[38:41], v[106:109], v[196:199], v[38:41]
	v_mfma_f32_16x16x32_bf16 v[30:33], v[114:117], v[196:199], v[30:33]
	v_mfma_f32_16x16x32_bf16 v[14:17], v[106:109], v[208:211], v[14:17]
	v_mfma_f32_16x16x32_bf16 v[10:13], v[114:117], v[208:211], v[10:13]
	v_mfma_f32_16x16x32_bf16 v[62:65], v[110:113], v[170:173], v[62:65]
	v_mfma_f32_16x16x32_bf16 v[58:61], v[118:121], v[170:173], v[58:61]
	v_mfma_f32_16x16x32_bf16 v[50:53], v[110:113], v[190:193], v[50:53]
	v_mfma_f32_16x16x32_bf16 v[42:45], v[118:121], v[190:193], v[42:45]
	v_mfma_f32_16x16x32_bf16 v[38:41], v[110:113], v[200:203], v[38:41]
	v_mfma_f32_16x16x32_bf16 v[30:33], v[118:121], v[200:203], v[30:33]
	v_mfma_f32_16x16x32_bf16 v[14:17], v[110:113], v[228:231], v[14:17]
	v_mfma_f32_16x16x32_bf16 v[10:13], v[118:121], v[228:231], v[10:13]
	s_barrier
	s_add_i32 s28, 0, 0x18000
	s_add_i32 s33, 0, 0x1c000
	v_add_u32_e32 v102, s28, v84
	v_add_u32_e32 v118, s33, v84
	ds_read_b128 v[90:93], v102
	ds_read_b128 v[94:97], v102 offset:1024
	ds_read_b128 v[98:101], v102 offset:2048
	ds_read_b128 v[102:105], v102 offset:3072
	ds_read_b128 v[106:109], v118
	ds_read_b128 v[110:113], v118 offset:1024
	ds_read_b128 v[114:117], v118 offset:2048
	ds_read_b128 v[118:121], v118 offset:3072
	s_mov_b32 m0, s66
	v_lshl_add_u64 v[238:239], s[48:49], 0, v[8:9]
	ds_read_b128 v[158:161], v85 offset:32768
	ds_read_b128 v[170:173], v85 offset:33792
	ds_read_b128 v[186:189], v85 offset:34816
	ds_read_b128 v[190:193], v85 offset:35840
	ds_read_b128 v[196:199], v85 offset:36864
	ds_read_b128 v[200:203], v85 offset:37888
	ds_read_b128 v[208:211], v85 offset:38912
	ds_read_b128 v[228:231], v85 offset:39936
	global_load_lds_dwordx4 v[238:239], off
	v_lshl_add_u64 v[238:239], s[48:49], 0, v[78:79]
	s_mov_b32 m0, s67
	s_nop 0
	global_load_lds_dwordx4 v[238:239], off
	s_waitcnt vmcnt(8)
	s_waitcnt lgkmcnt(0)
	s_barrier
	s_waitcnt lgkmcnt(0)
	v_mfma_f32_16x16x32_bf16 v[182:185], v[90:93], v[158:161], v[182:185]
	v_mfma_f32_16x16x32_bf16 v[178:181], v[98:101], v[158:161], v[178:181]
	v_mfma_f32_16x16x32_bf16 v[166:169], v[90:93], v[186:189], v[166:169]
	v_mfma_f32_16x16x32_bf16 v[162:165], v[98:101], v[186:189], v[162:165]
	v_mfma_f32_16x16x32_bf16 v[150:153], v[90:93], v[196:199], v[150:153]
	v_mfma_f32_16x16x32_bf16 v[146:149], v[98:101], v[196:199], v[146:149]
	v_mfma_f32_16x16x32_bf16 v[126:129], v[90:93], v[208:211], v[126:129]
	v_mfma_f32_16x16x32_bf16 v[122:125], v[98:101], v[208:211], v[122:125]
	v_mfma_f32_16x16x32_bf16 v[182:185], v[94:97], v[170:173], v[182:185]
	v_mfma_f32_16x16x32_bf16 v[178:181], v[102:105], v[170:173], v[178:181]
	v_mfma_f32_16x16x32_bf16 v[166:169], v[94:97], v[190:193], v[166:169]
	v_mfma_f32_16x16x32_bf16 v[162:165], v[102:105], v[190:193], v[162:165]
	v_mfma_f32_16x16x32_bf16 v[150:153], v[94:97], v[200:203], v[150:153]
	v_mfma_f32_16x16x32_bf16 v[146:149], v[102:105], v[200:203], v[146:149]
	v_mfma_f32_16x16x32_bf16 v[126:129], v[94:97], v[228:231], v[126:129]
	v_mfma_f32_16x16x32_bf16 v[122:125], v[102:105], v[228:231], v[122:125]
	v_mfma_f32_16x16x32_bf16 v[174:177], v[106:109], v[158:161], v[174:177]
	v_mfma_f32_16x16x32_bf16 v[130:133], v[114:117], v[158:161], v[130:133]
	v_mfma_f32_16x16x32_bf16 v[174:177], v[110:113], v[170:173], v[174:177]
	v_mfma_f32_16x16x32_bf16 v[170:173], v[118:121], v[170:173], v[130:133]
	v_mfma_f32_16x16x32_bf16 v[130:133], v[106:109], v[186:189], v[134:137]
	v_mfma_f32_16x16x32_bf16 v[158:161], v[110:113], v[190:193], v[130:133]
	v_mfma_f32_16x16x32_bf16 v[130:133], v[114:117], v[186:189], v[154:157]
	v_mfma_f32_16x16x32_bf16 v[154:157], v[118:121], v[190:193], v[130:133]
	v_mfma_f32_16x16x32_bf16 v[130:133], v[106:109], v[196:199], v[142:145]
	v_mfma_f32_16x16x32_bf16 v[142:145], v[110:113], v[200:203], v[130:133]
	v_mfma_f32_16x16x32_bf16 v[130:133], v[114:117], v[196:199], v[138:141]
	v_mfma_f32_16x16x32_bf16 v[86:89], v[106:109], v[208:211], v[86:89]
	v_mfma_f32_16x16x32_bf16 v[74:77], v[114:117], v[208:211], v[74:77]
	v_mfma_f32_16x16x32_bf16 v[138:141], v[118:121], v[200:203], v[130:133]
	v_mfma_f32_16x16x32_bf16 v[86:89], v[110:113], v[228:231], v[86:89]
	v_mfma_f32_16x16x32_bf16 v[74:77], v[118:121], v[228:231], v[74:77]
	s_barrier
; #define PG8_STAGE(bufoff, gbase, voff) do { _Pragma("unroll") for (int _i = 0; _i < 2; ++_i) \
;         __builtin_amdgcn_global_load_lds((const unsigned*)((const char*)(gbase) + (voff)[_i]), (LAS unsigned*)(lds + (bufoff) + ldsw + _i * 8192), 16, 0, 0); } while (0)
; #define PG8_LDA(dst, b, h) do { _Pragma("unroll") for (int m = 0; m < 4; ++m) _Pragma("unroll") for (int k = 0; k < 2; ++k) dst[m][k] = *(const LAS bf16x8*)(lds + PG8_SA(b, h) + aoff + m * 2048 + k * 1024); } while (0)
; #define PG8_MMA(ai, bj, At, Bt) do { __builtin_amdgcn_s_setprio(1); _Pragma("unroll") for (int m = 0; m < 4; ++m) _Pragma("unroll") for (int n = 0; n < 2; ++n) _Pragma("unroll") for (int k = 0; k < 2; ++k) \
;         acc[ai][bj][m][n] = __builtin_amdgcn_mfma_f32_16x16x32_bf16(Bt[n][k], At[m][k], acc[ai][bj][m][n], 0, 0, 0); __builtin_amdgcn_s_setprio(0); } while (0)
; #define PG8_WAIT_V(n) asm volatile("s_waitcnt vmcnt(" #n ")" ::: "memory")
; #define PG8_WAIT_L(n) asm volatile("s_waitcnt lgkmcnt(" #n ")" ::: "memory")
; #define PG8_BAR __builtin_amdgcn_s_barrier()
; #define PG8_SCHED __builtin_amdgcn_sched_barrier(0)
; template <class Epi, class Sched, bool GATHER = false>
; __device__ __forceinline__ void gemm_phase(LAS unsigned char* lds, const int lda, const int ldb, const int K, const Sched& S, const Epi& E, const int* gidx = nullptr) {
;     ...
;             PG8_LDA(At, 1, 1); PG8_STAGE(PG8_SB(1, 0), b3, voffB); PG8_STAGE(PG8_SB(1, 1), b3 + hstepB, voffB); PG8_STAGE(PG8_SA(1, 0), a3, o2[0]);
;             PG8_WAIT_V(8); PG8_WAIT_L(0); PG8_BAR; PG8_MMA(1, 0, At, B0); PG8_MMA(1, 1, At, B1); PG8_BAR; PG8_SCHED;
;         }
;         if (wr == 0) PG8_BAR;
	s_add_i32 s28, s28, s50
	v_lshl_add_u64 v[204:205], v[204:205], 0, s[64:65]
	s_mov_b32 m0, s28
	ds_read_b128 v[130:133], v85 offset:49152
	ds_read_b128 v[134:137], v85 offset:50176
	ds_read_b128 v[186:189], v85 offset:51200
	ds_read_b128 v[190:193], v85 offset:52224
	ds_read_b128 v[196:199], v85 offset:53248
	ds_read_b128 v[200:203], v85 offset:54272
	ds_read_b128 v[208:211], v85 offset:55296
	ds_read_b128 v[228:231], v85 offset:56320
	global_load_lds_dwordx4 v[204:205], off
	s_add_i32 m0, s28, 0x2000
	s_add_u32 s28, s34, 0x80080
	v_lshl_add_u64 v[204:205], v[232:233], 0, s[64:65]
	s_addc_u32 s29, s35, 0
	s_add_i32 s33, s33, s50
	global_load_lds_dwordx4 v[204:205], off
	v_lshl_add_u64 v[204:205], s[28:29], 0, v[194:195]
	s_mov_b32 m0, s33
	s_nop 0
	global_load_lds_dwordx4 v[204:205], off
	v_lshl_add_u64 v[204:205], s[28:29], 0, v[2:3]
	s_add_i32 m0, s33, 0x2000
	s_nop 0
	global_load_lds_dwordx4 v[204:205], off
	v_lshl_add_u64 v[204:205], v[234:235], 0, s[64:65]
	s_mov_b32 m0, s70
	s_nop 0
	global_load_lds_dwordx4 v[204:205], off
	v_lshl_add_u64 v[204:205], v[236:237], 0, s[64:65]
	s_mov_b32 m0, s71
	s_nop 0
	global_load_lds_dwordx4 v[204:205], off
	s_waitcnt vmcnt(8)
	s_waitcnt lgkmcnt(0)
	s_barrier
	s_waitcnt lgkmcnt(0)
	v_mfma_f32_16x16x32_bf16 v[70:73], v[90:93], v[130:133], v[70:73]
	v_mfma_f32_16x16x32_bf16 v[66:69], v[98:101], v[130:133], v[66:69]
	v_mfma_f32_16x16x32_bf16 v[54:57], v[90:93], v[186:189], v[54:57]
	v_mfma_f32_16x16x32_bf16 v[46:49], v[98:101], v[186:189], v[46:49]
	v_mfma_f32_16x16x32_bf16 v[34:37], v[90:93], v[196:199], v[34:37]
	v_mfma_f32_16x16x32_bf16 v[26:29], v[98:101], v[196:199], v[26:29]
	v_mfma_f32_16x16x32_bf16 v[22:25], v[90:93], v[208:211], v[22:25]
	v_mfma_f32_16x16x32_bf16 v[18:21], v[98:101], v[208:211], v[18:21]
	v_mfma_f32_16x16x32_bf16 v[70:73], v[94:97], v[134:137], v[70:73]
	v_mfma_f32_16x16x32_bf16 v[66:69], v[102:105], v[134:137], v[66:69]
	v_mfma_f32_16x16x32_bf16 v[54:57], v[94:97], v[190:193], v[54:57]
	v_mfma_f32_16x16x32_bf16 v[46:49], v[102:105], v[190:193], v[46:49]
	v_mfma_f32_16x16x32_bf16 v[34:37], v[94:97], v[200:203], v[34:37]
	v_mfma_f32_16x16x32_bf16 v[26:29], v[102:105], v[200:203], v[26:29]
	v_mfma_f32_16x16x32_bf16 v[22:25], v[94:97], v[228:231], v[22:25]
	v_mfma_f32_16x16x32_bf16 v[18:21], v[102:105], v[228:231], v[18:21]
	v_mfma_f32_16x16x32_bf16 v[62:65], v[106:109], v[130:133], v[62:65]
	v_mfma_f32_16x16x32_bf16 v[58:61], v[114:117], v[130:133], v[58:61]
	v_mfma_f32_16x16x32_bf16 v[50:53], v[106:109], v[186:189], v[50:53]
	v_mfma_f32_16x16x32_bf16 v[42:45], v[114:117], v[186:189], v[42:45]
	v_mfma_f32_16x16x32_bf16 v[38:41], v[106:109], v[196:199], v[38:41]
	v_mfma_f32_16x16x32_bf16 v[30:33], v[114:117], v[196:199], v[30:33]
	v_mfma_f32_16x16x32_bf16 v[14:17], v[106:109], v[208:211], v[14:17]
	v_mfma_f32_16x16x32_bf16 v[10:13], v[114:117], v[208:211], v[10:13]
	v_mfma_f32_16x16x32_bf16 v[62:65], v[110:113], v[134:137], v[62:65]
	v_mfma_f32_16x16x32_bf16 v[58:61], v[118:121], v[134:137], v[58:61]
	v_mfma_f32_16x16x32_bf16 v[50:53], v[110:113], v[190:193], v[50:53]
	v_mfma_f32_16x16x32_bf16 v[42:45], v[118:121], v[190:193], v[42:45]
	v_mfma_f32_16x16x32_bf16 v[38:41], v[110:113], v[200:203], v[38:41]
	v_mfma_f32_16x16x32_bf16 v[30:33], v[118:121], v[200:203], v[30:33]
	v_mfma_f32_16x16x32_bf16 v[14:17], v[110:113], v[228:231], v[14:17]
	v_mfma_f32_16x16x32_bf16 v[10:13], v[118:121], v[228:231], v[10:13]
	s_barrier
	s_add_i32 s72, s72, 2
	s_add_u32 s12, s12, 0x100
	s_addc_u32 s13, s13, 0
	s_cmp_gt_u32 s72, 29
	s_cbranch_scc0 .LBB0_1186
	s_cmpk_lt_u32 s8, 0x100
	s_cbranch_scc0 .LBB0_1189
	s_barrier

; #define PG8_AOFF(of, u) do { _Pragma("unroll") for (int hh_ = 0; hh_ < 2; ++hh_) _Pragma("unroll") for (int i_ = 0; i_ < 2; ++i_) { \
;         if constexpr (GATHER) of[hh_][i_] = (unsigned)gidx[(u).pm * 256 + hh_ * 128 + RA[i_]] * (unsigned)(lda * 2) + CA2[i_]; \
;         else of[hh_][i_] = (unsigned)((hh_ * HALF + RA[i_]) * lda) * 2u + CA2[i_]; } } while (0)
; #define PG8_STAGE(bufoff, gbase, voff) do { _Pragma("unroll") for (int _i = 0; _i < 2; ++_i) \
;         __builtin_amdgcn_global_load_lds((const unsigned*)((const char*)(gbase) + (voff)[_i]), (LAS unsigned*)(lds + (bufoff) + ldsw + _i * 8192), 16, 0, 0); } while (0)
; #define PG8_LDA(dst, b, h) do { _Pragma("unroll") for (int m = 0; m < 4; ++m) _Pragma("unroll") for (int k = 0; k < 2; ++k) dst[m][k] = *(const LAS bf16x8*)(lds + PG8_SA(b, h) + aoff + m * 2048 + k * 1024); } while (0)
; #define PG8_LDB(dst, b, h) do { _Pragma("unroll") for (int n = 0; n < 2; ++n) _Pragma("unroll") for (int k = 0; k < 2; ++k) dst[n][k] = *(const LAS bf16x8*)(lds + PG8_SB(b, h) + boff + n * 2048 + k * 1024); } while (0)
; template <class Epi, class Sched, bool GATHER = false>
; __device__ __forceinline__ void gemm_phase(LAS unsigned char* lds, const int lda, const int ldb, const int K, const Sched& S, const Epi& E, const int* gidx = nullptr) {
;     ...
;         for (int t = 0; t < nt; t += 2) {
;             const bool last = (t == nt - 2);
;             if constexpr (GATHER) { if (last && has_next) PG8_AOFF(ofn, nxt); }
;             const char* a1 = cA + (size_t)(t + 1) * kstep;
;             const char* a2 = last ? nA : cA + (size_t)(t + 2) * kstep; const char* b2 = last ? nB : cB + (size_t)(t + 2) * kstep;
;             const char* a3 = a2 + kstep; const char* b3 = b2 + kstep;
;             unsigned o2[2][2];
; #pragma unroll
;             for (int hh = 0; hh < 2; ++hh)
; #pragma unroll
;                 for (int i = 0; i < 2; ++i) { if constexpr (GATHER) o2[hh][i] = last ? ofn[hh][i] : ofc[hh][i]; else o2[hh][i] = ofc[hh][i]; }
;             PG8_LDB(B0, 0, 0); PG8_LDB(B1, 0, 1); PG8_SCHED; PG8_LDA(At, 0, 0); PG8_STAGE(PG8_SA(1, 1), a1, ofc[1]);
;             PG8_WAIT_V(8); PG8_WAIT_L(0); PG8_BAR; PG8_MMA(0, 0, At, B0); PG8_MMA(0, 1, At, B1); PG8_BAR; PG8_SCHED;
;             PG8_LDA(At, 0, 1); PG8_STAGE(PG8_SB(0, 0), b2, voffB); PG8_STAGE(PG8_SB(0, 1), b2 + hstepB, voffB); PG8_STAGE(PG8_SA(0, 0), a2, o2[0]);
.LBB0_1666:
	s_add_u32 s12, s26, s44
	s_addc_u32 s13, s27, s45
	s_add_u32 s28, s12, 0x24400100
	s_addc_u32 s29, s13, 0
	s_and_b64 s[12:13], s[34:35], exec
	s_cselect_b32 s49, s17, s29
	s_cselect_b32 s48, s16, s28
	s_add_u32 s28, s72, s44
	s_addc_u32 s29, s73, s45
	s_and_b64 s[12:13], s[34:35], exec
	s_cselect_b32 s13, s41, s29
	s_cselect_b32 s12, s40, s28
	s_add_i32 s28, 0, 0x10000
	v_add_u32_e32 v135, s28, v159
	s_add_i32 s33, 0, 0x14000
	ds_read_b128 v[164:167], v135
	ds_read_b128 v[168:171], v135 offset:1024
	ds_read_b128 v[172:175], v135 offset:2048
	ds_read_b128 v[176:179], v135 offset:3072
	v_add_u32_e32 v135, s33, v159
	ds_read_b128 v[180:183], v135
	ds_read_b128 v[184:187], v135 offset:1024
	ds_read_b128 v[188:191], v135 offset:2048
	ds_read_b128 v[196:199], v135 offset:3072
	v_cndmask_b32_e64 v194, v138, v141, s[34:35]
	v_cndmask_b32_e64 v192, v136, v143, s[34:35]
	v_cndmask_b32_e64 v135, v140, v161, s[34:35]
	v_cndmask_b32_e64 v137, v142, v162, s[34:35]
	v_lshl_add_u64 v[222:223], v[154:155], 0, s[44:45]
	s_add_i32 m0, s10, 0xc000
	ds_read_b128 v[200:203], v160
	ds_read_b128 v[204:207], v160 offset:1024
	ds_read_b128 v[208:211], v160 offset:2048
	ds_read_b128 v[228:231], v160 offset:3072
	ds_read_b128 v[232:235], v160 offset:4096
	ds_read_b128 v[236:239], v160 offset:5120
	ds_read_b128 v[240:243], v160 offset:6144
	ds_read_b128 v[244:247], v160 offset:7168
	global_load_lds_dwordx4 v[222:223], off
	v_lshl_add_u64 v[222:223], v[152:153], 0, s[44:45]
	s_add_i32 m0, s10, 0xe000
	s_nop 0
	global_load_lds_dwordx4 v[222:223], off
	s_waitcnt vmcnt(8)
	s_waitcnt lgkmcnt(0)
	s_barrier
	s_waitcnt lgkmcnt(0)
	v_mfma_f32_16x16x32_bf16 v[126:129], v[164:167], v[200:203], v[126:129]
	v_mfma_f32_16x16x32_bf16 v[118:121], v[172:175], v[200:203], v[118:121]
	v_mfma_f32_16x16x32_bf16 v[110:113], v[164:167], v[208:211], v[110:113]
	v_mfma_f32_16x16x32_bf16 v[102:105], v[172:175], v[208:211], v[102:105]
	v_mfma_f32_16x16x32_bf16 v[94:97], v[164:167], v[232:235], v[94:97]
	v_mfma_f32_16x16x32_bf16 v[86:89], v[172:175], v[232:235], v[86:89]
	v_mfma_f32_16x16x32_bf16 v[78:81], v[164:167], v[240:243], v[78:81]
	v_mfma_f32_16x16x32_bf16 v[70:73], v[172:175], v[240:243], v[70:73]
	v_mfma_f32_16x16x32_bf16 v[126:129], v[168:171], v[204:207], v[126:129]
	v_mfma_f32_16x16x32_bf16 v[118:121], v[176:179], v[204:207], v[118:121]
	v_mfma_f32_16x16x32_bf16 v[110:113], v[168:171], v[228:231], v[110:113]
	v_mfma_f32_16x16x32_bf16 v[102:105], v[176:179], v[228:231], v[102:105]
	v_mfma_f32_16x16x32_bf16 v[94:97], v[168:171], v[236:239], v[94:97]
	v_mfma_f32_16x16x32_bf16 v[86:89], v[176:179], v[236:239], v[86:89]
	v_mfma_f32_16x16x32_bf16 v[78:81], v[168:171], v[244:247], v[78:81]
	v_mfma_f32_16x16x32_bf16 v[70:73], v[176:179], v[244:247], v[70:73]
	v_mfma_f32_16x16x32_bf16 v[122:125], v[180:183], v[200:203], v[122:125]
	v_mfma_f32_16x16x32_bf16 v[114:117], v[188:191], v[200:203], v[114:117]
	v_mfma_f32_16x16x32_bf16 v[106:109], v[180:183], v[208:211], v[106:109]
	v_mfma_f32_16x16x32_bf16 v[98:101], v[188:191], v[208:211], v[98:101]
	v_mfma_f32_16x16x32_bf16 v[90:93], v[180:183], v[232:235], v[90:93]
	v_mfma_f32_16x16x32_bf16 v[82:85], v[188:191], v[232:235], v[82:85]
	v_mfma_f32_16x16x32_bf16 v[74:77], v[180:183], v[240:243], v[74:77]
	v_mfma_f32_16x16x32_bf16 v[66:69], v[188:191], v[240:243], v[66:69]
	v_mfma_f32_16x16x32_bf16 v[122:125], v[184:187], v[204:207], v[122:125]
	v_mfma_f32_16x16x32_bf16 v[114:117], v[196:199], v[204:207], v[114:117]
	v_mfma_f32_16x16x32_bf16 v[106:109], v[184:187], v[228:231], v[106:109]
	v_mfma_f32_16x16x32_bf16 v[98:101], v[196:199], v[228:231], v[98:101]
	v_mfma_f32_16x16x32_bf16 v[90:93], v[184:187], v[236:239], v[90:93]
	v_mfma_f32_16x16x32_bf16 v[82:85], v[196:199], v[236:239], v[82:85]
	v_mfma_f32_16x16x32_bf16 v[74:77], v[184:187], v[244:247], v[74:77]
	v_mfma_f32_16x16x32_bf16 v[66:69], v[196:199], v[244:247], v[66:69]
	s_barrier
	s_add_i32 s28, s28, s9
	v_lshl_add_u64 v[222:223], s[12:13], 0, v[130:131]
	s_mov_b32 m0, s28
	ds_read_b128 v[200:203], v160 offset:16384
	ds_read_b128 v[204:207], v160 offset:17408
	ds_read_b128 v[208:211], v160 offset:18432
	ds_read_b128 v[228:231], v160 offset:19456
	ds_read_b128 v[232:235], v160 offset:20480
	ds_read_b128 v[236:239], v160 offset:21504
	ds_read_b128 v[240:243], v160 offset:22528
	ds_read_b128 v[244:247], v160 offset:23552
	global_load_lds_dwordx4 v[222:223], off
	s_add_i32 m0, s28, 0x2000
	s_add_u32 s28, s12, 0x80000
	v_lshl_add_u64 v[224:225], s[12:13], 0, v[132:133]
	s_addc_u32 s29, s13, 0
	s_add_i32 s33, s33, s9
	global_load_lds_dwordx4 v[224:225], off
	v_lshl_add_u64 v[214:215], s[28:29], 0, v[130:131]
	s_mov_b32 m0, s33
	v_mov_b32_e32 v193, v195
	global_load_lds_dwordx4 v[214:215], off
	v_lshl_add_u64 v[214:215], s[28:29], 0, v[132:133]
	s_add_i32 m0, s33, 0x2000
	s_nop 0
	global_load_lds_dwordx4 v[214:215], off
	s_mov_b32 m0, s10
	v_lshl_add_u64 v[214:215], s[48:49], 0, v[194:195]
	global_load_lds_dwordx4 v194, s[48:49]
	s_mov_b32 m0, s11
	s_nop 0
	global_load_lds_dwordx4 v192, s[48:49]
	s_waitcnt vmcnt(8)
	s_waitcnt lgkmcnt(0)
	v_lshl_add_u64 v[192:193], s[48:49], 0, v[192:193]
	s_barrier
; #define PG8_STAGE(bufoff, gbase, voff) do { _Pragma("unroll") for (int _i = 0; _i < 2; ++_i) \
;         __builtin_amdgcn_global_load_lds((const unsigned*)((const char*)(gbase) + (voff)[_i]), (LAS unsigned*)(lds + (bufoff) + ldsw + _i * 8192), 16, 0, 0); } while (0)
; #define PG8_LDA(dst, b, h) do { _Pragma("unroll") for (int m = 0; m < 4; ++m) _Pragma("unroll") for (int k = 0; k < 2; ++k) dst[m][k] = *(const LAS bf16x8*)(lds + PG8_SA(b, h) + aoff + m * 2048 + k * 1024); } while (0)
; #define PG8_LDB(dst, b, h) do { _Pragma("unroll") for (int n = 0; n < 2; ++n) _Pragma("unroll") for (int k = 0; k < 2; ++k) dst[n][k] = *(const LAS bf16x8*)(lds + PG8_SB(b, h) + boff + n * 2048 + k * 1024); } while (0)
; #define PG8_MMA(ai, bj, At, Bt) do { __builtin_amdgcn_s_setprio(1); _Pragma("unroll") for (int m = 0; m < 4; ++m) _Pragma("unroll") for (int n = 0; n < 2; ++n) _Pragma("unroll") for (int k = 0; k < 2; ++k) \
;         acc[ai][bj][m][n] = __builtin_amdgcn_mfma_f32_16x16x32_bf16(Bt[n][k], At[m][k], acc[ai][bj][m][n], 0, 0, 0); __builtin_amdgcn_s_setprio(0); } while (0)
; #define PG8_WAIT_V(n) asm volatile("s_waitcnt vmcnt(" #n ")" ::: "memory")
; #define PG8_WAIT_L(n) asm volatile("s_waitcnt lgkmcnt(" #n ")" ::: "memory")
; #define PG8_BAR __builtin_amdgcn_s_barrier()
; #define PG8_SCHED __builtin_amdgcn_sched_barrier(0)
; template <class Epi, class Sched, bool GATHER = false>
; __device__ __forceinline__ void gemm_phase(LAS unsigned char* lds, const int lda, const int ldb, const int K, const Sched& S, const Epi& E, const int* gidx = nullptr) {
;     ...
;             PG8_WAIT_V(8); PG8_WAIT_L(0); PG8_BAR; PG8_MMA(1, 0, At, B0); PG8_MMA(1, 1, At, B1); PG8_BAR; PG8_SCHED;
;             PG8_LDB(B0, 1, 0); PG8_LDB(B1, 1, 1); PG8_SCHED; PG8_LDA(At, 1, 0); PG8_STAGE(PG8_SA(0, 1), a2, o2[1]);
;             PG8_WAIT_V(8); PG8_WAIT_L(0); PG8_BAR; PG8_MMA(0, 0, At, B0); PG8_MMA(0, 1, At, B1); PG8_BAR; PG8_SCHED;
	s_waitcnt lgkmcnt(0)
	v_mfma_f32_16x16x32_bf16 v[62:65], v[164:167], v[200:203], v[62:65]
	v_mfma_f32_16x16x32_bf16 v[54:57], v[172:175], v[200:203], v[54:57]
	v_mfma_f32_16x16x32_bf16 v[46:49], v[164:167], v[208:211], v[46:49]
	v_mfma_f32_16x16x32_bf16 v[38:41], v[172:175], v[208:211], v[38:41]
	v_mfma_f32_16x16x32_bf16 v[22:25], v[164:167], v[232:235], v[22:25]
	v_mfma_f32_16x16x32_bf16 v[18:21], v[172:175], v[232:235], v[18:21]
	v_mfma_f32_16x16x32_bf16 v[6:9], v[164:167], v[240:243], v[6:9]
	v_mfma_f32_16x16x32_bf16 v[2:5], v[172:175], v[240:243], v[2:5]
	v_mfma_f32_16x16x32_bf16 v[62:65], v[168:171], v[204:207], v[62:65]
	v_mfma_f32_16x16x32_bf16 v[54:57], v[176:179], v[204:207], v[54:57]
	v_mfma_f32_16x16x32_bf16 v[46:49], v[168:171], v[228:231], v[46:49]
	v_mfma_f32_16x16x32_bf16 v[38:41], v[176:179], v[228:231], v[38:41]
	v_mfma_f32_16x16x32_bf16 v[22:25], v[168:171], v[236:239], v[22:25]
	v_mfma_f32_16x16x32_bf16 v[18:21], v[176:179], v[236:239], v[18:21]
	v_mfma_f32_16x16x32_bf16 v[6:9], v[168:171], v[244:247], v[6:9]
	v_mfma_f32_16x16x32_bf16 v[2:5], v[176:179], v[244:247], v[2:5]
	v_mfma_f32_16x16x32_bf16 v[58:61], v[180:183], v[200:203], v[58:61]
	v_mfma_f32_16x16x32_bf16 v[50:53], v[188:191], v[200:203], v[50:53]
	v_mfma_f32_16x16x32_bf16 v[42:45], v[180:183], v[208:211], v[42:45]
	v_mfma_f32_16x16x32_bf16 v[34:37], v[188:191], v[208:211], v[34:37]
	v_mfma_f32_16x16x32_bf16 v[30:33], v[180:183], v[232:235], v[30:33]
	v_mfma_f32_16x16x32_bf16 v[26:29], v[188:191], v[232:235], v[26:29]
	v_mfma_f32_16x16x32_bf16 v[14:17], v[180:183], v[240:243], v[14:17]
	v_mfma_f32_16x16x32_bf16 v[10:13], v[188:191], v[240:243], v[10:13]
	v_mfma_f32_16x16x32_bf16 v[58:61], v[184:187], v[204:207], v[58:61]
	v_mfma_f32_16x16x32_bf16 v[50:53], v[196:199], v[204:207], v[50:53]
	v_mfma_f32_16x16x32_bf16 v[42:45], v[184:187], v[228:231], v[42:45]
	v_mfma_f32_16x16x32_bf16 v[34:37], v[196:199], v[228:231], v[34:37]
	v_mfma_f32_16x16x32_bf16 v[30:33], v[184:187], v[236:239], v[30:33]
	v_mfma_f32_16x16x32_bf16 v[26:29], v[196:199], v[236:239], v[26:29]
	v_mfma_f32_16x16x32_bf16 v[14:17], v[184:187], v[244:247], v[14:17]
	v_mfma_f32_16x16x32_bf16 v[10:13], v[196:199], v[244:247], v[10:13]
	s_barrier
	s_add_i32 s28, 0, 0x18000
	v_add_u32_e32 v163, s28, v159
	s_add_i32 s29, 0, 0x1c000
	ds_read_b128 v[164:167], v163
	ds_read_b128 v[168:171], v163 offset:1024
	ds_read_b128 v[172:175], v163 offset:2048
	ds_read_b128 v[176:179], v163 offset:3072
	v_add_u32_e32 v163, s29, v159
	ds_read_b128 v[180:183], v163
	ds_read_b128 v[184:187], v163 offset:1024
	ds_read_b128 v[188:191], v163 offset:2048
	ds_read_b128 v[196:199], v163 offset:3072
	s_mov_b32 m0, s22
	ds_read_b128 v[200:203], v160 offset:32768
	ds_read_b128 v[204:207], v160 offset:33792
	ds_read_b128 v[208:211], v160 offset:34816
	ds_read_b128 v[228:231], v160 offset:35840
	ds_read_b128 v[232:235], v160 offset:36864
	ds_read_b128 v[236:239], v160 offset:37888
	ds_read_b128 v[240:243], v160 offset:38912
	ds_read_b128 v[244:247], v160 offset:39936
	global_load_lds_dwordx4 v135, s[48:49]
	s_mov_b32 m0, s23
	s_nop 0
	global_load_lds_dwordx4 v137, s[48:49]
	s_waitcnt vmcnt(8)
	s_waitcnt lgkmcnt(0)
	s_barrier
	s_waitcnt lgkmcnt(0)
	v_mfma_f32_16x16x32_bf16 v[126:129], v[164:167], v[200:203], v[126:129]
	v_mfma_f32_16x16x32_bf16 v[118:121], v[172:175], v[200:203], v[118:121]
	v_mfma_f32_16x16x32_bf16 v[110:113], v[164:167], v[208:211], v[110:113]
	v_mfma_f32_16x16x32_bf16 v[102:105], v[172:175], v[208:211], v[102:105]
	v_mfma_f32_16x16x32_bf16 v[94:97], v[164:167], v[232:235], v[94:97]
	v_mfma_f32_16x16x32_bf16 v[86:89], v[172:175], v[232:235], v[86:89]
	v_mfma_f32_16x16x32_bf16 v[78:81], v[164:167], v[240:243], v[78:81]
	v_mfma_f32_16x16x32_bf16 v[70:73], v[172:175], v[240:243], v[70:73]
	v_mfma_f32_16x16x32_bf16 v[126:129], v[168:171], v[204:207], v[126:129]
	v_mfma_f32_16x16x32_bf16 v[118:121], v[176:179], v[204:207], v[118:121]
	v_mfma_f32_16x16x32_bf16 v[110:113], v[168:171], v[228:231], v[110:113]
	v_mfma_f32_16x16x32_bf16 v[102:105], v[176:179], v[228:231], v[102:105]
	v_mfma_f32_16x16x32_bf16 v[94:97], v[168:171], v[236:239], v[94:97]
	v_mfma_f32_16x16x32_bf16 v[86:89], v[176:179], v[236:239], v[86:89]
	v_mfma_f32_16x16x32_bf16 v[78:81], v[168:171], v[244:247], v[78:81]
	v_mfma_f32_16x16x32_bf16 v[70:73], v[176:179], v[244:247], v[70:73]
	v_mfma_f32_16x16x32_bf16 v[122:125], v[180:183], v[200:203], v[122:125]
	v_mfma_f32_16x16x32_bf16 v[114:117], v[188:191], v[200:203], v[114:117]
	v_mfma_f32_16x16x32_bf16 v[106:109], v[180:183], v[208:211], v[106:109]
	v_mfma_f32_16x16x32_bf16 v[98:101], v[188:191], v[208:211], v[98:101]
	v_mfma_f32_16x16x32_bf16 v[90:93], v[180:183], v[232:235], v[90:93]
	v_mfma_f32_16x16x32_bf16 v[82:85], v[188:191], v[232:235], v[82:85]
	v_mfma_f32_16x16x32_bf16 v[74:77], v[180:183], v[240:243], v[74:77]
	v_mfma_f32_16x16x32_bf16 v[66:69], v[188:191], v[240:243], v[66:69]
	v_mfma_f32_16x16x32_bf16 v[122:125], v[184:187], v[204:207], v[122:125]
	v_mfma_f32_16x16x32_bf16 v[114:117], v[196:199], v[204:207], v[114:117]
	v_mfma_f32_16x16x32_bf16 v[106:109], v[184:187], v[228:231], v[106:109]
	v_mfma_f32_16x16x32_bf16 v[98:101], v[196:199], v[228:231], v[98:101]
	v_mfma_f32_16x16x32_bf16 v[90:93], v[184:187], v[236:239], v[90:93]
	v_mfma_f32_16x16x32_bf16 v[82:85], v[196:199], v[236:239], v[82:85]
	v_mfma_f32_16x16x32_bf16 v[74:77], v[184:187], v[244:247], v[74:77]
	v_mfma_f32_16x16x32_bf16 v[66:69], v[196:199], v[244:247], v[66:69]
	s_barrier
; #define PG8_STAGE(bufoff, gbase, voff) do { _Pragma("unroll") for (int _i = 0; _i < 2; ++_i) \
;         __builtin_amdgcn_global_load_lds((const unsigned*)((const char*)(gbase) + (voff)[_i]), (LAS unsigned*)(lds + (bufoff) + ldsw + _i * 8192), 16, 0, 0); } while (0)
; #define PG8_LDA(dst, b, h) do { _Pragma("unroll") for (int m = 0; m < 4; ++m) _Pragma("unroll") for (int k = 0; k < 2; ++k) dst[m][k] = *(const LAS bf16x8*)(lds + PG8_SA(b, h) + aoff + m * 2048 + k * 1024); } while (0)
; #define PG8_MMA(ai, bj, At, Bt) do { __builtin_amdgcn_s_setprio(1); _Pragma("unroll") for (int m = 0; m < 4; ++m) _Pragma("unroll") for (int n = 0; n < 2; ++n) _Pragma("unroll") for (int k = 0; k < 2; ++k) \
;         acc[ai][bj][m][n] = __builtin_amdgcn_mfma_f32_16x16x32_bf16(Bt[n][k], At[m][k], acc[ai][bj][m][n], 0, 0, 0); __builtin_amdgcn_s_setprio(0); } while (0)
; #define PG8_WAIT_V(n) asm volatile("s_waitcnt vmcnt(" #n ")" ::: "memory")
; #define PG8_WAIT_L(n) asm volatile("s_waitcnt lgkmcnt(" #n ")" ::: "memory")
; #define PG8_BAR __builtin_amdgcn_s_barrier()
; #define PG8_SCHED __builtin_amdgcn_sched_barrier(0)
; template <class Epi, class Sched, bool GATHER = false>
; __device__ __forceinline__ void gemm_phase(LAS unsigned char* lds, const int lda, const int ldb, const int K, const Sched& S, const Epi& E, const int* gidx = nullptr) {
;     ...
;             PG8_LDA(At, 1, 1); PG8_STAGE(PG8_SB(1, 0), b3, voffB); PG8_STAGE(PG8_SB(1, 1), b3 + hstepB, voffB); PG8_STAGE(PG8_SA(1, 0), a3, o2[0]);
;             PG8_WAIT_V(8); PG8_WAIT_L(0); PG8_BAR; PG8_MMA(1, 0, At, B0); PG8_MMA(1, 1, At, B1); PG8_BAR; PG8_SCHED;
;         }
	s_add_i32 s28, s28, s9
	v_lshl_add_u64 v[222:223], v[222:223], 0, s[64:65]
	s_mov_b32 m0, s28
	ds_read_b128 v[200:203], v160 offset:49152
	ds_read_b128 v[204:207], v160 offset:50176
	ds_read_b128 v[208:211], v160 offset:51200
	ds_read_b128 v[228:231], v160 offset:52224
	ds_read_b128 v[232:235], v160 offset:53248
	ds_read_b128 v[236:239], v160 offset:54272
	ds_read_b128 v[240:243], v160 offset:55296
	ds_read_b128 v[244:247], v160 offset:56320
	global_load_lds_dwordx4 v[222:223], off
	s_add_i32 m0, s28, 0x2000
	s_add_u32 s12, s12, 0x80080
	v_lshl_add_u64 v[222:223], v[224:225], 0, s[64:65]
	s_addc_u32 s13, s13, 0
	s_add_i32 s28, s29, s9
	global_load_lds_dwordx4 v[222:223], off
	v_lshl_add_u64 v[222:223], s[12:13], 0, v[130:131]
	s_mov_b32 m0, s28
	v_lshl_add_u64 v[214:215], v[214:215], 0, s[64:65]
	global_load_lds_dwordx4 v[222:223], off
	v_lshl_add_u64 v[222:223], s[12:13], 0, v[132:133]
	s_add_i32 m0, s28, 0x2000
	v_lshl_add_u64 v[192:193], v[192:193], 0, s[64:65]
	global_load_lds_dwordx4 v[222:223], off
	s_mov_b32 m0, s50
	s_nop 0
	global_load_lds_dwordx4 v[214:215], off
	s_mov_b32 m0, s51
	s_nop 0
	global_load_lds_dwordx4 v[192:193], off
	s_waitcnt vmcnt(8)
	s_waitcnt lgkmcnt(0)
	s_barrier
	s_waitcnt lgkmcnt(0)
	v_mfma_f32_16x16x32_bf16 v[62:65], v[164:167], v[200:203], v[62:65]
	v_mfma_f32_16x16x32_bf16 v[54:57], v[172:175], v[200:203], v[54:57]
	v_mfma_f32_16x16x32_bf16 v[46:49], v[164:167], v[208:211], v[46:49]
	v_mfma_f32_16x16x32_bf16 v[38:41], v[172:175], v[208:211], v[38:41]
	v_mfma_f32_16x16x32_bf16 v[22:25], v[164:167], v[232:235], v[22:25]
	v_mfma_f32_16x16x32_bf16 v[18:21], v[172:175], v[232:235], v[18:21]
	v_mfma_f32_16x16x32_bf16 v[6:9], v[164:167], v[240:243], v[6:9]
	v_mfma_f32_16x16x32_bf16 v[2:5], v[172:175], v[240:243], v[2:5]
	v_mfma_f32_16x16x32_bf16 v[62:65], v[168:171], v[204:207], v[62:65]
	v_mfma_f32_16x16x32_bf16 v[54:57], v[176:179], v[204:207], v[54:57]
	v_mfma_f32_16x16x32_bf16 v[46:49], v[168:171], v[228:231], v[46:49]
	v_mfma_f32_16x16x32_bf16 v[38:41], v[176:179], v[228:231], v[38:41]
	v_mfma_f32_16x16x32_bf16 v[22:25], v[168:171], v[236:239], v[22:25]
	v_mfma_f32_16x16x32_bf16 v[18:21], v[176:179], v[236:239], v[18:21]
	v_mfma_f32_16x16x32_bf16 v[6:9], v[168:171], v[244:247], v[6:9]
	v_mfma_f32_16x16x32_bf16 v[2:5], v[176:179], v[244:247], v[2:5]
	v_mfma_f32_16x16x32_bf16 v[58:61], v[180:183], v[200:203], v[58:61]
	v_mfma_f32_16x16x32_bf16 v[50:53], v[188:191], v[200:203], v[50:53]
	v_mfma_f32_16x16x32_bf16 v[42:45], v[180:183], v[208:211], v[42:45]
	v_mfma_f32_16x16x32_bf16 v[34:37], v[188:191], v[208:211], v[34:37]
	v_mfma_f32_16x16x32_bf16 v[30:33], v[180:183], v[232:235], v[30:33]
	v_mfma_f32_16x16x32_bf16 v[26:29], v[188:191], v[232:235], v[26:29]
	v_mfma_f32_16x16x32_bf16 v[14:17], v[180:183], v[240:243], v[14:17]
	v_mfma_f32_16x16x32_bf16 v[10:13], v[188:191], v[240:243], v[10:13]
	v_mfma_f32_16x16x32_bf16 v[58:61], v[184:187], v[204:207], v[58:61]
	v_mfma_f32_16x16x32_bf16 v[50:53], v[196:199], v[204:207], v[50:53]
	v_mfma_f32_16x16x32_bf16 v[42:45], v[184:187], v[228:231], v[42:45]
	v_mfma_f32_16x16x32_bf16 v[34:37], v[196:199], v[228:231], v[34:37]
	v_mfma_f32_16x16x32_bf16 v[30:33], v[184:187], v[236:239], v[30:33]
	v_mfma_f32_16x16x32_bf16 v[26:29], v[196:199], v[236:239], v[26:29]
	v_mfma_f32_16x16x32_bf16 v[14:17], v[184:187], v[244:247], v[14:17]
	v_mfma_f32_16x16x32_bf16 v[10:13], v[196:199], v[244:247], v[10:13]
	s_barrier
	s_add_i32 s74, s74, 2
	s_add_u32 s44, s44, 0x100
	s_addc_u32 s45, s45, 0
	s_cmp_gt_u32 s74, 29
	s_cbranch_scc1 .LBB0_1669

; #define PG8_AOFF(of, u) do { _Pragma("unroll") for (int hh_ = 0; hh_ < 2; ++hh_) _Pragma("unroll") for (int i_ = 0; i_ < 2; ++i_) { \
;         if constexpr (GATHER) of[hh_][i_] = (unsigned)gidx[(u).pm * 256 + hh_ * 128 + RA[i_]] * (unsigned)(lda * 2) + CA2[i_]; \
;         else of[hh_][i_] = (unsigned)((hh_ * HALF + RA[i_]) * lda) * 2u + CA2[i_]; } } while (0)
; #define PG8_STAGE(bufoff, gbase, voff) do { _Pragma("unroll") for (int _i = 0; _i < 2; ++_i) \
;         __builtin_amdgcn_global_load_lds((const unsigned*)((const char*)(gbase) + (voff)[_i]), (LAS unsigned*)(lds + (bufoff) + ldsw + _i * 8192), 16, 0, 0); } while (0)
; #define PG8_LDA(dst, b, h) do { _Pragma("unroll") for (int m = 0; m < 4; ++m) _Pragma("unroll") for (int k = 0; k < 2; ++k) dst[m][k] = *(const LAS bf16x8*)(lds + PG8_SA(b, h) + aoff + m * 2048 + k * 1024); } while (0)
; #define PG8_LDB(dst, b, h) do { _Pragma("unroll") for (int n = 0; n < 2; ++n) _Pragma("unroll") for (int k = 0; k < 2; ++k) dst[n][k] = *(const LAS bf16x8*)(lds + PG8_SB(b, h) + boff + n * 2048 + k * 1024); } while (0)
; template <class Epi, class Sched, bool GATHER = false>
; __device__ __forceinline__ void gemm_phase(LAS unsigned char* lds, const int lda, const int ldb, const int K, const Sched& S, const Epi& E, const int* gidx = nullptr) {
;     ...
;         for (int t = 0; t < nt; t += 2) {
;             const bool last = (t == nt - 2);
;             if constexpr (GATHER) { if (last && has_next) PG8_AOFF(ofn, nxt); }
;             const char* a1 = cA + (size_t)(t + 1) * kstep;
;             const char* a2 = last ? nA : cA + (size_t)(t + 2) * kstep; const char* b2 = last ? nB : cB + (size_t)(t + 2) * kstep;
;             const char* a3 = a2 + kstep; const char* b3 = b2 + kstep;
;             unsigned o2[2][2];
; #pragma unroll
;             for (int hh = 0; hh < 2; ++hh)
; #pragma unroll
;                 for (int i = 0; i < 2; ++i) { if constexpr (GATHER) o2[hh][i] = last ? ofn[hh][i] : ofc[hh][i]; else o2[hh][i] = ofc[hh][i]; }
;             PG8_LDB(B0, 0, 0); PG8_LDB(B1, 0, 1); PG8_SCHED; PG8_LDA(At, 0, 0); PG8_STAGE(PG8_SA(1, 1), a1, ofc[1]);
;             PG8_WAIT_V(8); PG8_WAIT_L(0); PG8_BAR; PG8_MMA(0, 0, At, B0); PG8_MMA(0, 1, At, B1); PG8_BAR; PG8_SCHED;
;             PG8_LDA(At, 0, 1); PG8_STAGE(PG8_SB(0, 0), b2, voffB); PG8_STAGE(PG8_SB(0, 1), b2 + hstepB, voffB); PG8_STAGE(PG8_SA(0, 0), a2, o2[0]);
.LBB0_1733:
	s_add_u32 s12, s44, 0x80
	s_addc_u32 s13, s45, 0
	s_cmp_eq_u32 s72, 12
	s_cselect_b32 s49, s39, s13
	s_cselect_b32 s48, s38, s12
	s_cselect_b32 s13, s41, s71
	s_cselect_b32 s12, s40, s70
	s_add_i32 s28, 0, 0x10000
	v_add_u32_e32 v146, s28, v147
	s_add_i32 s33, 0, 0x14000
	ds_read_b128 v[152:155], v146
	ds_read_b128 v[156:159], v146 offset:1024
	ds_read_b128 v[160:163], v146 offset:2048
	ds_read_b128 v[164:167], v146 offset:3072
	v_add_u32_e32 v146, s33, v147
	ds_read_b128 v[168:171], v146
	ds_read_b128 v[172:175], v146 offset:1024
	ds_read_b128 v[176:179], v146 offset:2048
	ds_read_b128 v[180:183], v146 offset:3072
	v_lshl_add_u64 v[148:149], s[44:45], 0, v[144:145]
	s_add_i32 m0, s10, 0xc000
	ds_read_b128 v[184:187], v151
	ds_read_b128 v[188:191], v151 offset:1024
	ds_read_b128 v[196:199], v151 offset:2048
	ds_read_b128 v[200:203], v151 offset:3072
	ds_read_b128 v[204:207], v151 offset:4096
	ds_read_b128 v[208:211], v151 offset:5120
	ds_read_b128 v[228:231], v151 offset:6144
	ds_read_b128 v[232:235], v151 offset:7168
	global_load_lds_dwordx4 v[148:149], off
	v_lshl_add_u64 v[148:149], s[44:45], 0, v[142:143]
	s_add_i32 m0, s10, 0xe000
	s_nop 0
	global_load_lds_dwordx4 v[148:149], off
	s_waitcnt vmcnt(8)
	s_waitcnt lgkmcnt(0)
	s_barrier
	s_waitcnt lgkmcnt(0)
	v_mfma_f32_16x16x32_bf16 v[126:129], v[152:155], v[184:187], v[126:129]
	v_mfma_f32_16x16x32_bf16 v[122:125], v[160:163], v[184:187], v[122:125]
	v_mfma_f32_16x16x32_bf16 v[110:113], v[152:155], v[196:199], v[110:113]
	v_mfma_f32_16x16x32_bf16 v[106:109], v[160:163], v[196:199], v[106:109]
	v_mfma_f32_16x16x32_bf16 v[94:97], v[152:155], v[204:207], v[94:97]
	v_mfma_f32_16x16x32_bf16 v[90:93], v[160:163], v[204:207], v[90:93]
	v_mfma_f32_16x16x32_bf16 v[82:85], v[152:155], v[228:231], v[82:85]
	v_mfma_f32_16x16x32_bf16 v[74:77], v[160:163], v[228:231], v[74:77]
	v_mfma_f32_16x16x32_bf16 v[126:129], v[156:159], v[188:191], v[126:129]
	v_mfma_f32_16x16x32_bf16 v[122:125], v[164:167], v[188:191], v[122:125]
	v_mfma_f32_16x16x32_bf16 v[110:113], v[156:159], v[200:203], v[110:113]
	v_mfma_f32_16x16x32_bf16 v[106:109], v[164:167], v[200:203], v[106:109]
	v_mfma_f32_16x16x32_bf16 v[94:97], v[156:159], v[208:211], v[94:97]
	v_mfma_f32_16x16x32_bf16 v[90:93], v[164:167], v[208:211], v[90:93]
	v_mfma_f32_16x16x32_bf16 v[82:85], v[156:159], v[232:235], v[82:85]
	v_mfma_f32_16x16x32_bf16 v[74:77], v[164:167], v[232:235], v[74:77]
	v_mfma_f32_16x16x32_bf16 v[118:121], v[168:171], v[184:187], v[118:121]
	v_mfma_f32_16x16x32_bf16 v[114:117], v[176:179], v[184:187], v[114:117]
	v_mfma_f32_16x16x32_bf16 v[102:105], v[168:171], v[196:199], v[102:105]
	v_mfma_f32_16x16x32_bf16 v[98:101], v[176:179], v[196:199], v[98:101]
	v_mfma_f32_16x16x32_bf16 v[86:89], v[168:171], v[204:207], v[86:89]
	v_mfma_f32_16x16x32_bf16 v[78:81], v[176:179], v[204:207], v[78:81]
	v_mfma_f32_16x16x32_bf16 v[62:65], v[168:171], v[228:231], v[62:65]
	v_mfma_f32_16x16x32_bf16 v[58:61], v[176:179], v[228:231], v[58:61]
	v_mfma_f32_16x16x32_bf16 v[118:121], v[172:175], v[188:191], v[118:121]
	v_mfma_f32_16x16x32_bf16 v[114:117], v[180:183], v[188:191], v[114:117]
	v_mfma_f32_16x16x32_bf16 v[102:105], v[172:175], v[200:203], v[102:105]
	v_mfma_f32_16x16x32_bf16 v[98:101], v[180:183], v[200:203], v[98:101]
	v_mfma_f32_16x16x32_bf16 v[86:89], v[172:175], v[208:211], v[86:89]
	v_mfma_f32_16x16x32_bf16 v[78:81], v[180:183], v[208:211], v[78:81]
	v_mfma_f32_16x16x32_bf16 v[62:65], v[172:175], v[232:235], v[62:65]
	v_mfma_f32_16x16x32_bf16 v[58:61], v[180:183], v[232:235], v[58:61]
	s_barrier
	s_add_i32 s28, s28, s9
	v_lshl_add_u64 v[148:149], s[12:13], 0, v[132:133]
	s_mov_b32 m0, s28
	ds_read_b128 v[184:187], v151 offset:16384
	ds_read_b128 v[188:191], v151 offset:17408
	ds_read_b128 v[196:199], v151 offset:18432
	ds_read_b128 v[200:203], v151 offset:19456
	ds_read_b128 v[204:207], v151 offset:20480
	ds_read_b128 v[208:211], v151 offset:21504
	ds_read_b128 v[228:231], v151 offset:22528
	ds_read_b128 v[232:235], v151 offset:23552
	global_load_lds_dwordx4 v[148:149], off
	s_add_i32 m0, s28, 0x2000
	s_add_u32 s28, s12, 0x40000
	v_lshl_add_u64 v[192:193], s[12:13], 0, v[130:131]
	s_addc_u32 s29, s13, 0
	s_add_i32 s33, s33, s9
	global_load_lds_dwordx4 v[192:193], off
	v_lshl_add_u64 v[214:215], s[28:29], 0, v[132:133]
	s_mov_b32 m0, s33
	v_lshl_add_u64 v[222:223], s[48:49], 0, v[136:137]
	global_load_lds_dwordx4 v[214:215], off
	v_lshl_add_u64 v[214:215], s[28:29], 0, v[130:131]
	s_add_i32 m0, s33, 0x2000
	s_nop 0
	global_load_lds_dwordx4 v[214:215], off
	v_lshl_add_u64 v[214:215], s[48:49], 0, v[134:135]
	s_mov_b32 m0, s10
	s_nop 0
	global_load_lds_dwordx4 v[214:215], off
	s_mov_b32 m0, s11
	s_nop 0
	global_load_lds_dwordx4 v[222:223], off
	s_waitcnt vmcnt(8)
	s_waitcnt lgkmcnt(0)
	s_barrier
; #define PG8_STAGE(bufoff, gbase, voff) do { _Pragma("unroll") for (int _i = 0; _i < 2; ++_i) \
;         __builtin_amdgcn_global_load_lds((const unsigned*)((const char*)(gbase) + (voff)[_i]), (LAS unsigned*)(lds + (bufoff) + ldsw + _i * 8192), 16, 0, 0); } while (0)
; #define PG8_LDA(dst, b, h) do { _Pragma("unroll") for (int m = 0; m < 4; ++m) _Pragma("unroll") for (int k = 0; k < 2; ++k) dst[m][k] = *(const LAS bf16x8*)(lds + PG8_SA(b, h) + aoff + m * 2048 + k * 1024); } while (0)
; #define PG8_LDB(dst, b, h) do { _Pragma("unroll") for (int n = 0; n < 2; ++n) _Pragma("unroll") for (int k = 0; k < 2; ++k) dst[n][k] = *(const LAS bf16x8*)(lds + PG8_SB(b, h) + boff + n * 2048 + k * 1024); } while (0)
; #define PG8_MMA(ai, bj, At, Bt) do { __builtin_amdgcn_s_setprio(1); _Pragma("unroll") for (int m = 0; m < 4; ++m) _Pragma("unroll") for (int n = 0; n < 2; ++n) _Pragma("unroll") for (int k = 0; k < 2; ++k) \
;         acc[ai][bj][m][n] = __builtin_amdgcn_mfma_f32_16x16x32_bf16(Bt[n][k], At[m][k], acc[ai][bj][m][n], 0, 0, 0); __builtin_amdgcn_s_setprio(0); } while (0)
; #define PG8_WAIT_V(n) asm volatile("s_waitcnt vmcnt(" #n ")" ::: "memory")
; #define PG8_WAIT_L(n) asm volatile("s_waitcnt lgkmcnt(" #n ")" ::: "memory")
; #define PG8_BAR __builtin_amdgcn_s_barrier()
; #define PG8_SCHED __builtin_amdgcn_sched_barrier(0)
; template <class Epi, class Sched, bool GATHER = false>
; __device__ __forceinline__ void gemm_phase(LAS unsigned char* lds, const int lda, const int ldb, const int K, const Sched& S, const Epi& E, const int* gidx = nullptr) {
;     ...
;             PG8_WAIT_V(8); PG8_WAIT_L(0); PG8_BAR; PG8_MMA(1, 0, At, B0); PG8_MMA(1, 1, At, B1); PG8_BAR; PG8_SCHED;
;             PG8_LDB(B0, 1, 0); PG8_LDB(B1, 1, 1); PG8_SCHED; PG8_LDA(At, 1, 0); PG8_STAGE(PG8_SA(0, 1), a2, o2[1]);
;             PG8_WAIT_V(8); PG8_WAIT_L(0); PG8_BAR; PG8_MMA(0, 0, At, B0); PG8_MMA(0, 1, At, B1); PG8_BAR; PG8_SCHED;
	s_waitcnt lgkmcnt(0)
	v_mfma_f32_16x16x32_bf16 v[54:57], v[152:155], v[184:187], v[54:57]
	v_mfma_f32_16x16x32_bf16 v[50:53], v[160:163], v[184:187], v[50:53]
	v_mfma_f32_16x16x32_bf16 v[30:33], v[152:155], v[196:199], v[30:33]
	v_mfma_f32_16x16x32_bf16 v[26:29], v[160:163], v[196:199], v[26:29]
	v_mfma_f32_16x16x32_bf16 v[14:17], v[152:155], v[204:207], v[14:17]
	v_mfma_f32_16x16x32_bf16 v[10:13], v[160:163], v[204:207], v[10:13]
	v_mfma_f32_16x16x32_bf16 v[6:9], v[152:155], v[228:231], v[6:9]
	v_mfma_f32_16x16x32_bf16 v[2:5], v[160:163], v[228:231], v[2:5]
	v_mfma_f32_16x16x32_bf16 v[54:57], v[156:159], v[188:191], v[54:57]
	v_mfma_f32_16x16x32_bf16 v[50:53], v[164:167], v[188:191], v[50:53]
	v_mfma_f32_16x16x32_bf16 v[30:33], v[156:159], v[200:203], v[30:33]
	v_mfma_f32_16x16x32_bf16 v[26:29], v[164:167], v[200:203], v[26:29]
	v_mfma_f32_16x16x32_bf16 v[14:17], v[156:159], v[208:211], v[14:17]
	v_mfma_f32_16x16x32_bf16 v[10:13], v[164:167], v[208:211], v[10:13]
	v_mfma_f32_16x16x32_bf16 v[6:9], v[156:159], v[232:235], v[6:9]
	v_mfma_f32_16x16x32_bf16 v[2:5], v[164:167], v[232:235], v[2:5]
	v_mfma_f32_16x16x32_bf16 v[66:69], v[168:171], v[184:187], v[66:69]
	v_mfma_f32_16x16x32_bf16 v[70:73], v[176:179], v[184:187], v[70:73]
	v_mfma_f32_16x16x32_bf16 v[42:45], v[168:171], v[196:199], v[42:45]
	v_mfma_f32_16x16x32_bf16 v[46:49], v[176:179], v[196:199], v[46:49]
	v_mfma_f32_16x16x32_bf16 v[34:37], v[168:171], v[204:207], v[34:37]
	v_mfma_f32_16x16x32_bf16 v[38:41], v[176:179], v[204:207], v[38:41]
	v_mfma_f32_16x16x32_bf16 v[18:21], v[168:171], v[228:231], v[18:21]
	v_mfma_f32_16x16x32_bf16 v[22:25], v[176:179], v[228:231], v[22:25]
	v_mfma_f32_16x16x32_bf16 v[66:69], v[172:175], v[188:191], v[66:69]
	v_mfma_f32_16x16x32_bf16 v[70:73], v[180:183], v[188:191], v[70:73]
	v_mfma_f32_16x16x32_bf16 v[42:45], v[172:175], v[200:203], v[42:45]
	v_mfma_f32_16x16x32_bf16 v[46:49], v[180:183], v[200:203], v[46:49]
	v_mfma_f32_16x16x32_bf16 v[34:37], v[172:175], v[208:211], v[34:37]
	v_mfma_f32_16x16x32_bf16 v[38:41], v[180:183], v[208:211], v[38:41]
	v_mfma_f32_16x16x32_bf16 v[18:21], v[172:175], v[232:235], v[18:21]
	v_mfma_f32_16x16x32_bf16 v[22:25], v[180:183], v[232:235], v[22:25]
	s_barrier
	s_add_i32 s28, 0, 0x18000
	v_add_u32_e32 v146, s28, v147
	s_add_i32 s29, 0, 0x1c000
	ds_read_b128 v[152:155], v146
	ds_read_b128 v[156:159], v146 offset:1024
	ds_read_b128 v[160:163], v146 offset:2048
	ds_read_b128 v[164:167], v146 offset:3072
	v_add_u32_e32 v146, s29, v147
	ds_read_b128 v[168:171], v146
	ds_read_b128 v[172:175], v146 offset:1024
	ds_read_b128 v[176:179], v146 offset:2048
	ds_read_b128 v[180:183], v146 offset:3072
	s_mov_b32 m0, s22
	v_lshl_add_u64 v[224:225], s[48:49], 0, v[138:139]
	ds_read_b128 v[184:187], v151 offset:32768
	ds_read_b128 v[188:191], v151 offset:33792
	ds_read_b128 v[196:199], v151 offset:34816
	ds_read_b128 v[200:203], v151 offset:35840
	ds_read_b128 v[204:207], v151 offset:36864
	ds_read_b128 v[208:211], v151 offset:37888
	ds_read_b128 v[228:231], v151 offset:38912
	ds_read_b128 v[232:235], v151 offset:39936
	global_load_lds_dwordx4 v[224:225], off
	v_lshl_add_u64 v[224:225], s[48:49], 0, v[140:141]
	s_mov_b32 m0, s23
	s_nop 0
	global_load_lds_dwordx4 v[224:225], off
	s_waitcnt vmcnt(8)
	s_waitcnt lgkmcnt(0)
	s_barrier
	s_waitcnt lgkmcnt(0)
	v_mfma_f32_16x16x32_bf16 v[126:129], v[152:155], v[184:187], v[126:129]
	v_mfma_f32_16x16x32_bf16 v[122:125], v[160:163], v[184:187], v[122:125]
	v_mfma_f32_16x16x32_bf16 v[110:113], v[152:155], v[196:199], v[110:113]
	v_mfma_f32_16x16x32_bf16 v[106:109], v[160:163], v[196:199], v[106:109]
	v_mfma_f32_16x16x32_bf16 v[94:97], v[152:155], v[204:207], v[94:97]
	v_mfma_f32_16x16x32_bf16 v[90:93], v[160:163], v[204:207], v[90:93]
	v_mfma_f32_16x16x32_bf16 v[82:85], v[152:155], v[228:231], v[82:85]
	v_mfma_f32_16x16x32_bf16 v[74:77], v[160:163], v[228:231], v[74:77]
	v_mfma_f32_16x16x32_bf16 v[126:129], v[156:159], v[188:191], v[126:129]
	v_mfma_f32_16x16x32_bf16 v[122:125], v[164:167], v[188:191], v[122:125]
	v_mfma_f32_16x16x32_bf16 v[110:113], v[156:159], v[200:203], v[110:113]
	v_mfma_f32_16x16x32_bf16 v[106:109], v[164:167], v[200:203], v[106:109]
	v_mfma_f32_16x16x32_bf16 v[94:97], v[156:159], v[208:211], v[94:97]
	v_mfma_f32_16x16x32_bf16 v[90:93], v[164:167], v[208:211], v[90:93]
	v_mfma_f32_16x16x32_bf16 v[82:85], v[156:159], v[232:235], v[82:85]
	v_mfma_f32_16x16x32_bf16 v[74:77], v[164:167], v[232:235], v[74:77]
	v_mfma_f32_16x16x32_bf16 v[118:121], v[168:171], v[184:187], v[118:121]
	v_mfma_f32_16x16x32_bf16 v[114:117], v[176:179], v[184:187], v[114:117]
	v_mfma_f32_16x16x32_bf16 v[102:105], v[168:171], v[196:199], v[102:105]
	v_mfma_f32_16x16x32_bf16 v[98:101], v[176:179], v[196:199], v[98:101]
	v_mfma_f32_16x16x32_bf16 v[86:89], v[168:171], v[204:207], v[86:89]
	v_mfma_f32_16x16x32_bf16 v[78:81], v[176:179], v[204:207], v[78:81]
	v_mfma_f32_16x16x32_bf16 v[62:65], v[168:171], v[228:231], v[62:65]
	v_mfma_f32_16x16x32_bf16 v[58:61], v[176:179], v[228:231], v[58:61]
	v_mfma_f32_16x16x32_bf16 v[118:121], v[172:175], v[188:191], v[118:121]
	v_mfma_f32_16x16x32_bf16 v[114:117], v[180:183], v[188:191], v[114:117]
	v_mfma_f32_16x16x32_bf16 v[102:105], v[172:175], v[200:203], v[102:105]
	v_mfma_f32_16x16x32_bf16 v[98:101], v[180:183], v[200:203], v[98:101]
	v_mfma_f32_16x16x32_bf16 v[86:89], v[172:175], v[208:211], v[86:89]
	v_mfma_f32_16x16x32_bf16 v[78:81], v[180:183], v[208:211], v[78:81]
	v_mfma_f32_16x16x32_bf16 v[62:65], v[172:175], v[232:235], v[62:65]
	v_mfma_f32_16x16x32_bf16 v[58:61], v[180:183], v[232:235], v[58:61]
	s_barrier
; #define PG8_STAGE(bufoff, gbase, voff) do { _Pragma("unroll") for (int _i = 0; _i < 2; ++_i) \
;         __builtin_amdgcn_global_load_lds((const unsigned*)((const char*)(gbase) + (voff)[_i]), (LAS unsigned*)(lds + (bufoff) + ldsw + _i * 8192), 16, 0, 0); } while (0)
; #define PG8_LDA(dst, b, h) do { _Pragma("unroll") for (int m = 0; m < 4; ++m) _Pragma("unroll") for (int k = 0; k < 2; ++k) dst[m][k] = *(const LAS bf16x8*)(lds + PG8_SA(b, h) + aoff + m * 2048 + k * 1024); } while (0)
; #define PG8_MMA(ai, bj, At, Bt) do { __builtin_amdgcn_s_setprio(1); _Pragma("unroll") for (int m = 0; m < 4; ++m) _Pragma("unroll") for (int n = 0; n < 2; ++n) _Pragma("unroll") for (int k = 0; k < 2; ++k) \
;         acc[ai][bj][m][n] = __builtin_amdgcn_mfma_f32_16x16x32_bf16(Bt[n][k], At[m][k], acc[ai][bj][m][n], 0, 0, 0); __builtin_amdgcn_s_setprio(0); } while (0)
; #define PG8_WAIT_V(n) asm volatile("s_waitcnt vmcnt(" #n ")" ::: "memory")
; #define PG8_WAIT_L(n) asm volatile("s_waitcnt lgkmcnt(" #n ")" ::: "memory")
; #define PG8_BAR __builtin_amdgcn_s_barrier()
; #define PG8_SCHED __builtin_amdgcn_sched_barrier(0)
; template <class Epi, class Sched, bool GATHER = false>
; __device__ __forceinline__ void gemm_phase(LAS unsigned char* lds, const int lda, const int ldb, const int K, const Sched& S, const Epi& E, const int* gidx = nullptr) {
;     ...
;             PG8_LDA(At, 1, 1); PG8_STAGE(PG8_SB(1, 0), b3, voffB); PG8_STAGE(PG8_SB(1, 1), b3 + hstepB, voffB); PG8_STAGE(PG8_SA(1, 0), a3, o2[0]);
;             PG8_WAIT_V(8); PG8_WAIT_L(0); PG8_BAR; PG8_MMA(1, 0, At, B0); PG8_MMA(1, 1, At, B1); PG8_BAR; PG8_SCHED;
;         }
;         if (wr == 0) PG8_BAR;
	s_add_i32 s28, s28, s9
	v_lshl_add_u64 v[148:149], v[148:149], 0, s[64:65]
	s_mov_b32 m0, s28
	ds_read_b128 v[184:187], v151 offset:49152
	ds_read_b128 v[188:191], v151 offset:50176
	ds_read_b128 v[196:199], v151 offset:51200
	ds_read_b128 v[200:203], v151 offset:52224
	ds_read_b128 v[204:207], v151 offset:53248
	ds_read_b128 v[208:211], v151 offset:54272
	ds_read_b128 v[228:231], v151 offset:55296
	ds_read_b128 v[232:235], v151 offset:56320
	global_load_lds_dwordx4 v[148:149], off
	s_add_i32 m0, s28, 0x2000
	s_add_u32 s12, s12, 0x40080
	v_lshl_add_u64 v[148:149], v[192:193], 0, s[64:65]
	s_addc_u32 s13, s13, 0
	s_add_i32 s28, s29, s9
	global_load_lds_dwordx4 v[148:149], off
	v_lshl_add_u64 v[148:149], s[12:13], 0, v[132:133]
	s_mov_b32 m0, s28
	s_nop 0
	global_load_lds_dwordx4 v[148:149], off
	v_lshl_add_u64 v[148:149], s[12:13], 0, v[130:131]
	s_add_i32 m0, s28, 0x2000
	s_nop 0
	global_load_lds_dwordx4 v[148:149], off
	v_lshl_add_u64 v[148:149], v[214:215], 0, s[64:65]
	s_mov_b32 m0, s50
	s_nop 0
	global_load_lds_dwordx4 v[148:149], off
	v_lshl_add_u64 v[148:149], v[222:223], 0, s[64:65]
	s_mov_b32 m0, s51
	s_nop 0
	global_load_lds_dwordx4 v[148:149], off
	s_waitcnt vmcnt(8)
	s_waitcnt lgkmcnt(0)
	s_barrier
	s_waitcnt lgkmcnt(0)
	v_mfma_f32_16x16x32_bf16 v[54:57], v[152:155], v[184:187], v[54:57]
	v_mfma_f32_16x16x32_bf16 v[50:53], v[160:163], v[184:187], v[50:53]
	v_mfma_f32_16x16x32_bf16 v[30:33], v[152:155], v[196:199], v[30:33]
	v_mfma_f32_16x16x32_bf16 v[26:29], v[160:163], v[196:199], v[26:29]
	v_mfma_f32_16x16x32_bf16 v[14:17], v[152:155], v[204:207], v[14:17]
	v_mfma_f32_16x16x32_bf16 v[10:13], v[160:163], v[204:207], v[10:13]
	v_mfma_f32_16x16x32_bf16 v[6:9], v[152:155], v[228:231], v[6:9]
	v_mfma_f32_16x16x32_bf16 v[2:5], v[160:163], v[228:231], v[2:5]
	v_mfma_f32_16x16x32_bf16 v[54:57], v[156:159], v[188:191], v[54:57]
	v_mfma_f32_16x16x32_bf16 v[50:53], v[164:167], v[188:191], v[50:53]
	v_mfma_f32_16x16x32_bf16 v[30:33], v[156:159], v[200:203], v[30:33]
	v_mfma_f32_16x16x32_bf16 v[26:29], v[164:167], v[200:203], v[26:29]
	v_mfma_f32_16x16x32_bf16 v[14:17], v[156:159], v[208:211], v[14:17]
	v_mfma_f32_16x16x32_bf16 v[10:13], v[164:167], v[208:211], v[10:13]
	v_mfma_f32_16x16x32_bf16 v[6:9], v[156:159], v[232:235], v[6:9]
	v_mfma_f32_16x16x32_bf16 v[2:5], v[164:167], v[232:235], v[2:5]
	v_mfma_f32_16x16x32_bf16 v[66:69], v[168:171], v[184:187], v[66:69]
	v_mfma_f32_16x16x32_bf16 v[70:73], v[176:179], v[184:187], v[70:73]
	v_mfma_f32_16x16x32_bf16 v[42:45], v[168:171], v[196:199], v[42:45]
	v_mfma_f32_16x16x32_bf16 v[46:49], v[176:179], v[196:199], v[46:49]
	v_mfma_f32_16x16x32_bf16 v[34:37], v[168:171], v[204:207], v[34:37]
	v_mfma_f32_16x16x32_bf16 v[38:41], v[176:179], v[204:207], v[38:41]
	v_mfma_f32_16x16x32_bf16 v[18:21], v[168:171], v[228:231], v[18:21]
	v_mfma_f32_16x16x32_bf16 v[22:25], v[176:179], v[228:231], v[22:25]
	v_mfma_f32_16x16x32_bf16 v[66:69], v[172:175], v[188:191], v[66:69]
	v_mfma_f32_16x16x32_bf16 v[70:73], v[180:183], v[188:191], v[70:73]
	v_mfma_f32_16x16x32_bf16 v[42:45], v[172:175], v[200:203], v[42:45]
	v_mfma_f32_16x16x32_bf16 v[46:49], v[180:183], v[200:203], v[46:49]
	v_mfma_f32_16x16x32_bf16 v[34:37], v[172:175], v[208:211], v[34:37]
	v_mfma_f32_16x16x32_bf16 v[38:41], v[180:183], v[208:211], v[38:41]
	v_mfma_f32_16x16x32_bf16 v[18:21], v[172:175], v[232:235], v[18:21]
	v_mfma_f32_16x16x32_bf16 v[22:25], v[180:183], v[232:235], v[22:25]
	s_barrier
	s_add_i32 s72, s72, 2
	s_add_u32 s44, s44, 0x100
	s_addc_u32 s45, s45, 0
	s_add_u32 s70, s70, 0x100
	s_addc_u32 s71, s71, 0
	s_cmp_gt_u32 s72, 13
	s_cbranch_scc0 .LBB0_1733
	s_and_b64 vcc, exec, s[36:37]
	s_cbranch_vccz .LBB0_1736
	s_barrier
